# workgroups without a router-GEMM tile (P11) convert the last expert-weight chunk of every workgroup; P4/P6 convert 7 chunks
# baseline (speedup 1.0000x reference)
.LBB0_1371:
	s_or_b64 exec, exec, s[12:13]
	s_waitcnt lgkmcnt(0)
	v_lshl_add_u32 v58, v72, 4, s54
	s_waitcnt lgkmcnt(0)
	ds_read_b32 v59, v58 offset:128
	s_lshl_b32 s0, s9, 8
	s_add_i32 s0, s0, 0
	v_lshl_add_u32 v60, v73, 2, s0
	s_lshl_b32 s0, s38, 10
	v_lshl_or_b32 v61, v72, 12, s0
	v_add_u32_e32 v62, v60, v61
	s_waitcnt lgkmcnt(0)
	v_mul_f32_e32 v4, v4, v59
	v_mul_f32_e32 v20, v20, v59
	ds_write2_b32 v62, v4, v20 offset1:32
	ds_read_b32 v4, v58 offset:132
	v_or_b32_e32 v20, 0x400, v61
	v_add_u32_e32 v20, v60, v20
	s_add_u32 s6, s31, s28
	s_addc_u32 s7, s33, 0
	s_waitcnt lgkmcnt(0)
	v_mul_f32_e32 v5, v5, v4
	v_mul_f32_e32 v4, v21, v4
	ds_write2_b32 v20, v5, v4 offset1:32
	ds_read_b32 v4, v58 offset:136
	v_or_b32_e32 v5, 0x800, v61
	v_add_u32_e32 v5, v60, v5
	s_mov_b32 s12, 0x358637bd
	s_lshl_b64 s[10:11], s[10:11], 12
	s_waitcnt lgkmcnt(0)
	v_mul_f32_e32 v6, v6, v4
	v_mul_f32_e32 v4, v22, v4
	ds_write2_b32 v5, v6, v4 offset1:32
	ds_read_b32 v4, v58 offset:140
	v_or_b32_e32 v5, 0xc00, v61
	v_add_u32_e32 v5, v60, v5
	s_waitcnt lgkmcnt(0)
	v_mul_f32_e32 v6, v7, v4
	v_mul_f32_e32 v4, v23, v4
	ds_write2_b32 v5, v6, v4 offset1:32
	ds_read_b32 v4, v58 offset:160
	v_or_b32_e32 v5, 0x2000, v61
	v_add_u32_e32 v5, v60, v5
	s_waitcnt vmcnt(8)
	v_and_b32_e32 v23, 0xffff0000, v54
	v_mul_f32_e32 v23, 0xbfb8aa3b, v23
	s_waitcnt lgkmcnt(0)
	v_mul_f32_e32 v6, v8, v4
	v_mul_f32_e32 v4, v24, v4
	ds_write2_b32 v5, v6, v4 offset1:32
	ds_read_b32 v4, v58 offset:164
	v_or_b32_e32 v5, 0x2400, v61
	v_add_u32_e32 v5, v60, v5
	v_or_b32_e32 v8, 0x4c00, v61
	v_add_u32_e32 v8, v60, v8
	s_waitcnt lgkmcnt(0)
	v_mul_f32_e32 v6, v9, v4
	v_mul_f32_e32 v4, v25, v4
	ds_write2_b32 v5, v6, v4 offset1:32
	ds_read_b32 v4, v58 offset:168
	v_or_b32_e32 v5, 0x2800, v61
	v_add_u32_e32 v5, v60, v5
	v_exp_f32_e32 v23, v23
	s_waitcnt lgkmcnt(0)
	v_mul_f32_e32 v6, v10, v4
	v_mul_f32_e32 v4, v26, v4
	ds_write2_b32 v5, v6, v4 offset1:32
	ds_read_b32 v4, v58 offset:172
	v_or_b32_e32 v5, 0x2c00, v61
	v_add_u32_e32 v5, v60, v5
	s_waitcnt lgkmcnt(0)
	v_mul_f32_e32 v6, v11, v4
	v_mul_f32_e32 v4, v27, v4
	ds_write2_b32 v5, v6, v4 offset1:32
	ds_read_b32 v4, v58 offset:192
	v_or_b32_e32 v5, 0x4000, v61
	v_add_u32_e32 v5, v60, v5
	s_waitcnt lgkmcnt(0)
	v_mul_f32_e32 v6, v12, v4
	v_mul_f32_e32 v4, v28, v4
	ds_write2_b32 v5, v6, v4 offset1:32
	ds_read_b32 v4, v58 offset:196
	v_or_b32_e32 v5, 0x4400, v61
	v_add_u32_e32 v5, v60, v5
	s_waitcnt lgkmcnt(0)
	v_mul_f32_e32 v6, v13, v4
	v_mul_f32_e32 v4, v29, v4
	ds_write2_b32 v5, v6, v4 offset1:32
	ds_read_b32 v4, v58 offset:200
	v_or_b32_e32 v6, 0x4800, v61
	v_add_u32_e32 v6, v60, v6
	v_lshlrev_b32_e32 v5, 2, v74
	v_lshl_add_u32 v21, v5, 2, 0
	s_waitcnt lgkmcnt(0)
	v_mul_f32_e32 v7, v14, v4
	v_mul_f32_e32 v4, v30, v4
	ds_write2_b32 v6, v7, v4 offset1:32
	ds_read_b32 v4, v58 offset:204
	v_xor_b32_e32 v6, 1, v111
	v_xor_b32_e32 v7, 2, v111
	v_cmp_lt_i32_e32 vcc, v6, v2
	s_waitcnt lgkmcnt(0)
	v_mul_f32_e32 v9, v15, v4
	v_mul_f32_e32 v4, v31, v4
	ds_write2_b32 v8, v9, v4 offset1:32
	ds_read_b32 v4, v58 offset:224
	v_or_b32_e32 v9, 0x6000, v61
	v_add_u32_e32 v9, v60, v9
	v_cndmask_b32_e32 v6, v111, v6, vcc
	v_cmp_lt_i32_e32 vcc, v7, v2
	s_waitcnt lgkmcnt(0)
	v_mul_f32_e32 v10, v16, v4
	v_mul_f32_e32 v4, v32, v4
	ds_write2_b32 v9, v10, v4 offset1:32
	ds_read_b32 v4, v58 offset:228
	v_or_b32_e32 v9, 0x6400, v61
	v_add_u32_e32 v9, v60, v9
	v_xor_b32_e32 v8, 4, v111
	v_cndmask_b32_e32 v7, v111, v7, vcc
	s_waitcnt lgkmcnt(0)
	v_mul_f32_e32 v10, v17, v4
	v_mul_f32_e32 v4, v33, v4
	ds_write2_b32 v9, v10, v4 offset1:32
	ds_read_b32 v4, v58 offset:232
	v_or_b32_e32 v9, 0x6800, v61
	v_add_u32_e32 v9, v60, v9
	v_lshlrev_b32_e32 v20, 2, v6
	v_cmp_lt_i32_e32 vcc, v8, v2
	s_waitcnt lgkmcnt(0)
	v_mul_f32_e32 v10, v18, v4
	v_mul_f32_e32 v4, v34, v4
	ds_write2_b32 v9, v10, v4 offset1:32
	ds_read_b32 v4, v58 offset:236
	v_or_b32_e32 v9, 0x6c00, v61
	v_lshlrev_b32_e32 v18, 2, v7
	v_add_u32_e32 v6, v60, v9
	s_waitcnt lgkmcnt(0)
	v_mul_f32_e32 v7, v19, v4
	v_mul_f32_e32 v4, v35, v4
	ds_write2_b32 v6, v7, v4 offset1:32
	v_cndmask_b32_e32 v4, v111, v8, vcc
	v_lshlrev_b32_e32 v22, 2, v4
	v_xor_b32_e32 v4, 8, v111
	v_cmp_lt_i32_e32 vcc, v4, v2
	s_waitcnt lgkmcnt(0)
	s_barrier
	s_nop 1
	v_cndmask_b32_e32 v2, v111, v4, vcc
	v_lshlrev_b32_e32 v19, 2, v2
	v_lshlrev_b32_e32 v2, 1, v5
	v_lshl_add_u32 v4, s25, 13, v21
	ds_read_b128 v[8:11], v4
	v_lshl_add_u64 v[12:13], s[6:7], 0, v[2:3]
	s_or_b32 s6, s24, 1
	v_lshl_add_u32 v2, s6, 10, v21
	ds_read_b128 v[4:7], v2
	s_waitcnt lgkmcnt(1)
	v_pk_mul_f32 v[14:15], v[10:11], v[10:11]
	v_pk_mul_f32 v[16:17], v[8:9], v[8:9]
	v_lshlrev_b32_e32 v2, 16, v54
	v_pk_mov_b32 v[24:25], v[16:17], v[14:15] op_sel:[1,0]
	v_mov_b32_e32 v17, v15
	v_pk_add_f32 v[14:15], v[24:25], v[16:17]
	s_waitcnt lgkmcnt(0)
	v_pk_mul_f32 v[16:17], v[6:7], v[6:7]
	v_pk_mul_f32 v[24:25], v[4:5], v[4:5]
	v_mul_f32_e32 v2, 0xbfb8aa3b, v2
	v_pk_mov_b32 v[26:27], v[24:25], v[16:17] op_sel:[1,0]
	v_mov_b32_e32 v25, v17
	v_pk_add_f32 v[16:17], v[26:27], v[24:25]
	v_mov_b32_e32 v25, v14
	v_mov_b32_e32 v24, v16
	v_mov_b32_e32 v14, v17
	v_pk_add_f32 v[14:15], v[24:25], v[14:15]
	ds_bpermute_b32 v17, v20, v15
	ds_bpermute_b32 v16, v20, v14
	v_exp_f32_e32 v2, v2
	v_and_b32_e32 v25, 0xffff0000, v55
	v_mul_f32_e32 v25, 0xbfb8aa3b, v25
	v_exp_f32_e32 v27, v25
	s_waitcnt lgkmcnt(0)
	v_pk_add_f32 v[14:15], v[14:15], v[16:17]
	ds_bpermute_b32 v17, v18, v15
	ds_bpermute_b32 v16, v18, v14
	v_add_f32_e32 v2, 1.0, v2
	v_rcp_f32_e32 v24, v2
	v_add_f32_e32 v2, 1.0, v23
	v_lshlrev_b32_e32 v23, 16, v55
	s_waitcnt lgkmcnt(0)
	v_pk_add_f32 v[14:15], v[14:15], v[16:17]
	ds_bpermute_b32 v17, v22, v15
	ds_bpermute_b32 v16, v22, v14
	v_mul_f32_e32 v23, 0xbfb8aa3b, v23
	v_exp_f32_e32 v23, v23
	v_rcp_f32_e32 v26, v2
	v_mov_b32_e32 v28, v8
	s_waitcnt lgkmcnt(0)
	v_pk_add_f32 v[14:15], v[14:15], v[16:17]
	ds_bpermute_b32 v17, v19, v15
	ds_bpermute_b32 v16, v19, v14
	v_add_f32_e32 v2, 1.0, v23
	v_rcp_f32_e32 v25, v2
	v_mov_b32_e32 v29, v10
	v_add_f32_e32 v2, 1.0, v27
	s_waitcnt lgkmcnt(0)
	v_pk_add_f32 v[14:15], v[14:15], v[16:17]
	ds_bpermute_b32 v17, v57, v15
	ds_bpermute_b32 v16, v57, v14
	v_pk_mul_f32 v[24:25], v[24:25], v[28:29]
	v_rcp_f32_e32 v27, v2
	v_mov_b32_e32 v10, v9
	s_ashr_i32 s0, s6, 31
	s_waitcnt lgkmcnt(0)
	v_pk_add_f32 v[16:17], v[14:15], v[16:17]
	ds_bpermute_b32 v29, v56, v17
	ds_bpermute_b32 v28, v56, v16
	v_pk_mul_f32 v[8:9], v[26:27], v[10:11]
	s_waitcnt vmcnt(0)
	v_mov_b32_e32 v15, v38
	v_mov_b32_e32 v38, v37
	v_mov_b32_e32 v14, v36
	s_waitcnt lgkmcnt(0)
	v_pk_add_f32 v[10:11], v[16:17], v[28:29]
	v_mov_b64_e32 v[16:17], s[12:13]
	v_pk_fma_f32 v[10:11], v[10:11], s[80:81], v[16:17] op_sel_hi:[1,0,0]
	v_lshl_add_u64 v[26:27], v[12:13], 0, s[10:11]
	v_mul_f32_e32 v2, 0x4b800000, v11
	v_cmp_gt_f32_e32 vcc, s19, v11
	s_add_u32 s6, s6, s8
	s_addc_u32 s7, s0, 0
	v_cndmask_b32_e32 v2, v11, v2, vcc
	v_rsq_f32_e32 v2, v2
	s_or_b32 s0, s24, 2
	s_lshl_b64 s[10:11], s[6:7], 12
	s_ashr_i32 s1, s0, 31
	v_mul_f32_e32 v11, 0x45800000, v2
	v_cndmask_b32_e32 v2, v2, v11, vcc
	v_pk_mul_f32 v[8:9], v[8:9], v[2:3] op_sel_hi:[1,0]
	v_pk_mul_f32 v[24:25], v[24:25], v[2:3] op_sel_hi:[1,0]
	v_pk_mul_f32 v[8:9], v[38:39], v[8:9]
	v_cmp_gt_f32_e32 vcc, s19, v10
	v_and_b32_sdwa v23, v9, v113 dst_sel:DWORD dst_unused:UNUSED_PAD src0_sel:WORD_1 src1_sel:DWORD
	v_add3_u32 v9, v9, v23, s20
	v_mul_f32_e32 v23, 0x4b800000, v10
	v_pk_mul_f32 v[24:25], v[14:15], v[24:25]
	v_cndmask_b32_e32 v10, v10, v23, vcc
	v_and_b32_sdwa v11, v24, v113 dst_sel:DWORD dst_unused:UNUSED_PAD src0_sel:WORD_1 src1_sel:DWORD
	v_rsq_f32_e32 v10, v10
	v_add3_u32 v11, v24, v11, s20
	v_and_b32_sdwa v24, v8, v113 dst_sel:DWORD dst_unused:UNUSED_PAD src0_sel:WORD_1 src1_sel:DWORD
	v_and_b32_sdwa v2, v25, v113 dst_sel:DWORD dst_unused:UNUSED_PAD src0_sel:WORD_1 src1_sel:DWORD
	v_add3_u32 v8, v8, v24, s20
	v_add3_u32 v2, v25, v2, s20
	v_and_b32_e32 v9, 0xffff0000, v9
	v_and_b32_e32 v8, 0xffff0000, v8
	v_or_b32_sdwa v9, v9, v2 dst_sel:DWORD dst_unused:UNUSED_PAD src0_sel:DWORD src1_sel:WORD_1
	v_or_b32_sdwa v8, v8, v11 dst_sel:DWORD dst_unused:UNUSED_PAD src0_sel:DWORD src1_sel:WORD_1
	v_mul_f32_e32 v2, 0x45800000, v10
	global_store_dwordx2 v[26:27], v[8:9], off
	v_cndmask_b32_e32 v2, v10, v2, vcc
	v_and_b32_e32 v9, 0xffff0000, v52
	v_lshlrev_b32_e32 v10, 16, v53
	v_lshlrev_b32_e32 v8, 16, v52
	v_mul_f32_e32 v9, 0xbfb8aa3b, v9
	v_mul_f32_e32 v10, 0xbfb8aa3b, v10
	v_mul_f32_e32 v8, 0xbfb8aa3b, v8
	v_exp_f32_e32 v9, v9
	v_exp_f32_e32 v11, v10
	v_and_b32_e32 v10, 0xffff0000, v53
	v_exp_f32_e32 v8, v8
	v_mul_f32_e32 v10, 0xbfb8aa3b, v10
	v_exp_f32_e32 v23, v10
	v_add_f32_e32 v9, 1.0, v9
	v_add_f32_e32 v8, 1.0, v8
	v_rcp_f32_e32 v10, v9
	v_add_f32_e32 v9, 1.0, v11
	v_rcp_f32_e32 v8, v8
	v_rcp_f32_e32 v9, v9
	v_add_f32_e32 v11, 1.0, v23
	v_rcp_f32_e32 v11, v11
	v_mov_b32_e32 v24, v4
	v_mov_b32_e32 v25, v6
	v_pk_mul_f32 v[8:9], v[8:9], v[24:25]
	v_mov_b32_e32 v6, v5
	v_pk_mul_f32 v[8:9], v[8:9], v[2:3] op_sel_hi:[1,0]
	v_pk_mul_f32 v[4:5], v[10:11], v[6:7]
	v_pk_mul_f32 v[8:9], v[14:15], v[8:9]
	v_pk_mul_f32 v[4:5], v[4:5], v[2:3] op_sel_hi:[1,0]
	v_and_b32_sdwa v6, v8, v113 dst_sel:DWORD dst_unused:UNUSED_PAD src0_sel:WORD_1 src1_sel:DWORD
	v_pk_mul_f32 v[4:5], v[38:39], v[4:5]
	v_add3_u32 v23, v8, v6, s20
	v_and_b32_sdwa v6, v5, v113 dst_sel:DWORD dst_unused:UNUSED_PAD src0_sel:WORD_1 src1_sel:DWORD
	v_and_b32_sdwa v2, v9, v113 dst_sel:DWORD dst_unused:UNUSED_PAD src0_sel:WORD_1 src1_sel:DWORD
	v_add3_u32 v5, v5, v6, s20
	v_add3_u32 v2, v9, v2, s20
	v_and_b32_sdwa v7, v4, v113 dst_sel:DWORD dst_unused:UNUSED_PAD src0_sel:WORD_1 src1_sel:DWORD
	v_and_b32_e32 v5, 0xffff0000, v5
	v_add3_u32 v4, v4, v7, s20
	v_or_b32_sdwa v25, v5, v2 dst_sel:DWORD dst_unused:UNUSED_PAD src0_sel:DWORD src1_sel:WORD_1
	v_lshl_add_u32 v2, s0, 10, v21
	s_add_u32 s6, s0, s8
	v_and_b32_e32 v24, 0xffff0000, v4
	ds_read_b128 v[4:7], v2
	s_addc_u32 s7, s1, 0
	s_or_b32 s9, s24, 3
	v_lshl_add_u32 v2, s9, 10, v21
	ds_read_b128 v[8:11], v2
	s_waitcnt lgkmcnt(1)
	v_pk_mul_f32 v[26:27], v[6:7], v[6:7]
	v_pk_mul_f32 v[28:29], v[4:5], v[4:5]
	v_or_b32_sdwa v24, v24, v23 dst_sel:DWORD dst_unused:UNUSED_PAD src0_sel:DWORD src1_sel:WORD_1
	v_pk_mov_b32 v[30:31], v[28:29], v[26:27] op_sel:[1,0]
	v_mov_b32_e32 v29, v27
	v_pk_add_f32 v[26:27], v[30:31], v[28:29]
	s_waitcnt lgkmcnt(0)
	v_pk_mul_f32 v[28:29], v[10:11], v[10:11]
	v_pk_mul_f32 v[30:31], v[8:9], v[8:9]
	v_lshlrev_b32_e32 v2, 16, v50
	v_pk_mov_b32 v[32:33], v[30:31], v[28:29] op_sel:[1,0]
	v_mov_b32_e32 v31, v29
	v_pk_add_f32 v[28:29], v[32:33], v[30:31]
	v_mov_b32_e32 v31, v26
	v_mov_b32_e32 v30, v28
	v_mov_b32_e32 v26, v29
	v_pk_add_f32 v[26:27], v[30:31], v[26:27]
	ds_bpermute_b32 v29, v20, v27
	ds_bpermute_b32 v28, v20, v26
	v_lshl_add_u64 v[30:31], v[12:13], 0, s[10:11]
	global_store_dwordx2 v[30:31], v[24:25], off
	v_mul_f32_e32 v2, 0xbfb8aa3b, v2
	v_exp_f32_e32 v2, v2
	s_waitcnt lgkmcnt(0)
	v_pk_add_f32 v[24:25], v[26:27], v[28:29]
	ds_bpermute_b32 v27, v18, v25
	ds_bpermute_b32 v26, v18, v24
	v_add_f32_e32 v2, 1.0, v2
	v_rcp_f32_e32 v28, v2
	v_and_b32_e32 v2, 0xffff0000, v50
	v_mul_f32_e32 v2, 0xbfb8aa3b, v2
	s_waitcnt lgkmcnt(0)
	v_pk_add_f32 v[24:25], v[24:25], v[26:27]
	ds_bpermute_b32 v27, v22, v25
	ds_bpermute_b32 v26, v22, v24
	v_exp_f32_e32 v2, v2
	v_and_b32_e32 v23, 0xffff0000, v51
	v_mul_f32_e32 v23, 0xbfb8aa3b, v23
	v_exp_f32_e32 v23, v23
	s_waitcnt lgkmcnt(0)
	v_pk_add_f32 v[24:25], v[24:25], v[26:27]
	ds_bpermute_b32 v27, v19, v25
	ds_bpermute_b32 v26, v19, v24
	v_add_f32_e32 v2, 1.0, v2
	v_rcp_f32_e32 v30, v2
	v_lshlrev_b32_e32 v2, 16, v51
	v_mul_f32_e32 v2, 0xbfb8aa3b, v2
	s_waitcnt lgkmcnt(0)
	v_pk_add_f32 v[24:25], v[24:25], v[26:27]
	ds_bpermute_b32 v27, v57, v25
	ds_bpermute_b32 v26, v57, v24
	v_exp_f32_e32 v2, v2
	v_mov_b32_e32 v32, v4
	v_mov_b32_e32 v33, v6
	v_mov_b32_e32 v6, v5
	s_waitcnt lgkmcnt(0)
	v_pk_add_f32 v[24:25], v[24:25], v[26:27]
	ds_bpermute_b32 v27, v56, v25
	ds_bpermute_b32 v26, v56, v24
	v_add_f32_e32 v2, 1.0, v2
	v_rcp_f32_e32 v29, v2
	v_add_f32_e32 v2, 1.0, v23
	v_rcp_f32_e32 v31, v2
	s_waitcnt lgkmcnt(0)
	v_pk_add_f32 v[4:5], v[24:25], v[26:27]
	v_pk_mul_f32 v[28:29], v[28:29], v[32:33]
	v_pk_fma_f32 v[4:5], v[4:5], s[80:81], v[16:17] op_sel_hi:[1,0,0]
	v_pk_mul_f32 v[6:7], v[30:31], v[6:7]
	v_mul_f32_e32 v2, 0x4b800000, v5
	v_cmp_gt_f32_e32 vcc, s19, v5
	s_lshl_b64 s[6:7], s[6:7], 12
	v_lshl_add_u64 v[24:25], v[12:13], 0, s[6:7]
	v_cndmask_b32_e32 v2, v5, v2, vcc
	v_rsq_f32_e32 v2, v2
	s_ashr_i32 s0, s9, 31
	s_add_u32 s6, s9, s8
	s_addc_u32 s7, s0, 0
	v_mul_f32_e32 v5, 0x45800000, v2
	v_cndmask_b32_e32 v2, v2, v5, vcc
	v_pk_mul_f32 v[26:27], v[28:29], v[2:3] op_sel_hi:[1,0]
	v_pk_mul_f32 v[6:7], v[6:7], v[2:3] op_sel_hi:[1,0]
	v_pk_mul_f32 v[26:27], v[14:15], v[26:27]
	v_pk_mul_f32 v[6:7], v[38:39], v[6:7]
	v_and_b32_sdwa v5, v26, v113 dst_sel:DWORD dst_unused:UNUSED_PAD src0_sel:WORD_1 src1_sel:DWORD
	v_add3_u32 v23, v26, v5, s20
	v_and_b32_sdwa v5, v7, v113 dst_sel:DWORD dst_unused:UNUSED_PAD src0_sel:WORD_1 src1_sel:DWORD
	v_add3_u32 v5, v7, v5, s20
	v_mul_f32_e32 v7, 0x4b800000, v4
	v_cmp_gt_f32_e32 vcc, s19, v4
	v_and_b32_sdwa v26, v6, v113 dst_sel:DWORD dst_unused:UNUSED_PAD src0_sel:WORD_1 src1_sel:DWORD
	v_and_b32_sdwa v2, v27, v113 dst_sel:DWORD dst_unused:UNUSED_PAD src0_sel:WORD_1 src1_sel:DWORD
	v_cndmask_b32_e32 v4, v4, v7, vcc
	v_add3_u32 v6, v6, v26, s20
	v_rsq_f32_e32 v7, v4
	v_add3_u32 v2, v27, v2, s20
	v_and_b32_e32 v5, 0xffff0000, v5
	v_and_b32_e32 v6, 0xffff0000, v6
	v_or_b32_sdwa v5, v5, v2 dst_sel:DWORD dst_unused:UNUSED_PAD src0_sel:DWORD src1_sel:WORD_1
	v_or_b32_sdwa v4, v6, v23 dst_sel:DWORD dst_unused:UNUSED_PAD src0_sel:DWORD src1_sel:WORD_1
	global_store_dwordx2 v[24:25], v[4:5], off
	v_and_b32_e32 v5, 0xffff0000, v48
	v_lshlrev_b32_e32 v6, 16, v49
	v_mul_f32_e32 v2, 0x45800000, v7
	v_lshlrev_b32_e32 v4, 16, v48
	v_mul_f32_e32 v5, 0xbfb8aa3b, v5
	v_mul_f32_e32 v6, 0xbfb8aa3b, v6
	v_cndmask_b32_e32 v2, v7, v2, vcc
	v_mul_f32_e32 v4, 0xbfb8aa3b, v4
	v_exp_f32_e32 v5, v5
	v_exp_f32_e32 v7, v6
	v_and_b32_e32 v6, 0xffff0000, v49
	v_exp_f32_e32 v4, v4
	v_mul_f32_e32 v6, 0xbfb8aa3b, v6
	v_exp_f32_e32 v23, v6
	v_add_f32_e32 v5, 1.0, v5
	v_add_f32_e32 v4, 1.0, v4
	v_rcp_f32_e32 v6, v5
	v_add_f32_e32 v5, 1.0, v7
	v_rcp_f32_e32 v4, v4
	v_rcp_f32_e32 v5, v5
	v_add_f32_e32 v7, 1.0, v23
	v_rcp_f32_e32 v7, v7
	v_mov_b32_e32 v24, v8
	v_mov_b32_e32 v25, v10
	v_pk_mul_f32 v[4:5], v[4:5], v[24:25]
	v_mov_b32_e32 v10, v9
	v_pk_mul_f32 v[4:5], v[4:5], v[2:3] op_sel_hi:[1,0]
	v_pk_mul_f32 v[6:7], v[6:7], v[10:11]
	v_pk_mul_f32 v[4:5], v[14:15], v[4:5]
	v_pk_mul_f32 v[6:7], v[6:7], v[2:3] op_sel_hi:[1,0]
	v_and_b32_sdwa v8, v4, v113 dst_sel:DWORD dst_unused:UNUSED_PAD src0_sel:WORD_1 src1_sel:DWORD
	v_pk_mul_f32 v[6:7], v[38:39], v[6:7]
	v_add3_u32 v23, v4, v8, s20
	v_and_b32_sdwa v4, v7, v113 dst_sel:DWORD dst_unused:UNUSED_PAD src0_sel:WORD_1 src1_sel:DWORD
	v_and_b32_sdwa v2, v5, v113 dst_sel:DWORD dst_unused:UNUSED_PAD src0_sel:WORD_1 src1_sel:DWORD
	v_add3_u32 v4, v7, v4, s20
	s_or_b32 s0, s24, 4
	v_add3_u32 v2, v5, v2, s20
	v_and_b32_sdwa v5, v6, v113 dst_sel:DWORD dst_unused:UNUSED_PAD src0_sel:WORD_1 src1_sel:DWORD
	v_and_b32_e32 v4, 0xffff0000, v4
	s_lshl_b64 s[10:11], s[6:7], 12
	s_ashr_i32 s1, s0, 31
	v_add3_u32 v5, v6, v5, s20
	v_or_b32_sdwa v25, v4, v2 dst_sel:DWORD dst_unused:UNUSED_PAD src0_sel:DWORD src1_sel:WORD_1
	v_lshl_add_u32 v2, s0, 10, v21
	s_add_u32 s6, s0, s8
	v_and_b32_e32 v24, 0xffff0000, v5
	ds_read_b128 v[4:7], v2
	s_addc_u32 s7, s1, 0
	s_or_b32 s9, s24, 5
	v_lshl_add_u32 v2, s9, 10, v21
	ds_read_b128 v[8:11], v2
	s_waitcnt lgkmcnt(1)
	v_pk_mul_f32 v[26:27], v[6:7], v[6:7]
	v_pk_mul_f32 v[28:29], v[4:5], v[4:5]
	v_or_b32_sdwa v24, v24, v23 dst_sel:DWORD dst_unused:UNUSED_PAD src0_sel:DWORD src1_sel:WORD_1
	v_pk_mov_b32 v[30:31], v[28:29], v[26:27] op_sel:[1,0]
	v_mov_b32_e32 v29, v27
	v_pk_add_f32 v[26:27], v[30:31], v[28:29]
	s_waitcnt lgkmcnt(0)
	v_pk_mul_f32 v[28:29], v[10:11], v[10:11]
	v_pk_mul_f32 v[30:31], v[8:9], v[8:9]
	v_lshlrev_b32_e32 v2, 16, v46
	v_pk_mov_b32 v[32:33], v[30:31], v[28:29] op_sel:[1,0]
	v_mov_b32_e32 v31, v29
	v_pk_add_f32 v[28:29], v[32:33], v[30:31]
	v_mov_b32_e32 v31, v26
	v_mov_b32_e32 v30, v28
	v_mov_b32_e32 v26, v29
	v_pk_add_f32 v[26:27], v[30:31], v[26:27]
	ds_bpermute_b32 v29, v20, v27
	ds_bpermute_b32 v28, v20, v26
	v_lshl_add_u64 v[30:31], v[12:13], 0, s[10:11]
	global_store_dwordx2 v[30:31], v[24:25], off
	v_mul_f32_e32 v2, 0xbfb8aa3b, v2
	v_exp_f32_e32 v2, v2
	s_waitcnt lgkmcnt(0)
	v_pk_add_f32 v[24:25], v[26:27], v[28:29]
	ds_bpermute_b32 v27, v18, v25
	ds_bpermute_b32 v26, v18, v24
	v_add_f32_e32 v2, 1.0, v2
	v_rcp_f32_e32 v28, v2
	v_and_b32_e32 v2, 0xffff0000, v46
	v_mul_f32_e32 v2, 0xbfb8aa3b, v2
	s_waitcnt lgkmcnt(0)
	v_pk_add_f32 v[24:25], v[24:25], v[26:27]
	ds_bpermute_b32 v27, v22, v25
	ds_bpermute_b32 v26, v22, v24
	v_exp_f32_e32 v2, v2
	v_and_b32_e32 v23, 0xffff0000, v47
	v_mul_f32_e32 v23, 0xbfb8aa3b, v23
	v_exp_f32_e32 v23, v23
	s_waitcnt lgkmcnt(0)
	v_pk_add_f32 v[24:25], v[24:25], v[26:27]
	ds_bpermute_b32 v27, v19, v25
	ds_bpermute_b32 v26, v19, v24
	v_add_f32_e32 v2, 1.0, v2
	v_rcp_f32_e32 v30, v2
	v_lshlrev_b32_e32 v2, 16, v47
	v_mul_f32_e32 v2, 0xbfb8aa3b, v2
	s_waitcnt lgkmcnt(0)
	v_pk_add_f32 v[24:25], v[24:25], v[26:27]
	ds_bpermute_b32 v27, v57, v25
	ds_bpermute_b32 v26, v57, v24
	v_exp_f32_e32 v2, v2
	v_mov_b32_e32 v32, v4
	v_mov_b32_e32 v33, v6
	v_mov_b32_e32 v6, v5
	s_waitcnt lgkmcnt(0)
	v_pk_add_f32 v[24:25], v[24:25], v[26:27]
	ds_bpermute_b32 v27, v56, v25
	ds_bpermute_b32 v26, v56, v24
	v_add_f32_e32 v2, 1.0, v2
	v_rcp_f32_e32 v29, v2
	v_add_f32_e32 v2, 1.0, v23
	v_rcp_f32_e32 v31, v2
	s_waitcnt lgkmcnt(0)
	v_pk_add_f32 v[4:5], v[24:25], v[26:27]
	v_pk_mul_f32 v[28:29], v[28:29], v[32:33]
	v_pk_fma_f32 v[4:5], v[4:5], s[80:81], v[16:17] op_sel_hi:[1,0,0]
	v_pk_mul_f32 v[6:7], v[30:31], v[6:7]
	v_mul_f32_e32 v2, 0x4b800000, v5
	v_cmp_gt_f32_e32 vcc, s19, v5
	s_lshl_b64 s[6:7], s[6:7], 12
	v_lshl_add_u64 v[24:25], v[12:13], 0, s[6:7]
	v_cndmask_b32_e32 v2, v5, v2, vcc
	v_rsq_f32_e32 v2, v2
	s_ashr_i32 s0, s9, 31
	s_add_u32 s6, s9, s8
	s_addc_u32 s7, s0, 0
	v_mul_f32_e32 v5, 0x45800000, v2
	v_cndmask_b32_e32 v2, v2, v5, vcc
	v_pk_mul_f32 v[26:27], v[28:29], v[2:3] op_sel_hi:[1,0]
	v_pk_mul_f32 v[6:7], v[6:7], v[2:3] op_sel_hi:[1,0]
	v_pk_mul_f32 v[26:27], v[14:15], v[26:27]
	v_pk_mul_f32 v[6:7], v[38:39], v[6:7]
	v_and_b32_sdwa v5, v26, v113 dst_sel:DWORD dst_unused:UNUSED_PAD src0_sel:WORD_1 src1_sel:DWORD
	v_add3_u32 v23, v26, v5, s20
	v_and_b32_sdwa v5, v7, v113 dst_sel:DWORD dst_unused:UNUSED_PAD src0_sel:WORD_1 src1_sel:DWORD
	v_add3_u32 v5, v7, v5, s20
	v_mul_f32_e32 v7, 0x4b800000, v4
	v_cmp_gt_f32_e32 vcc, s19, v4
	v_and_b32_sdwa v26, v6, v113 dst_sel:DWORD dst_unused:UNUSED_PAD src0_sel:WORD_1 src1_sel:DWORD
	v_and_b32_sdwa v2, v27, v113 dst_sel:DWORD dst_unused:UNUSED_PAD src0_sel:WORD_1 src1_sel:DWORD
	v_cndmask_b32_e32 v4, v4, v7, vcc
	v_add3_u32 v6, v6, v26, s20
	v_rsq_f32_e32 v7, v4
	v_add3_u32 v2, v27, v2, s20
	v_and_b32_e32 v5, 0xffff0000, v5
	v_and_b32_e32 v6, 0xffff0000, v6
	v_or_b32_sdwa v5, v5, v2 dst_sel:DWORD dst_unused:UNUSED_PAD src0_sel:DWORD src1_sel:WORD_1
	v_or_b32_sdwa v4, v6, v23 dst_sel:DWORD dst_unused:UNUSED_PAD src0_sel:DWORD src1_sel:WORD_1
	global_store_dwordx2 v[24:25], v[4:5], off
	v_and_b32_e32 v5, 0xffff0000, v44
	v_lshlrev_b32_e32 v6, 16, v45
	v_mul_f32_e32 v2, 0x45800000, v7
	v_lshlrev_b32_e32 v4, 16, v44
	v_mul_f32_e32 v5, 0xbfb8aa3b, v5
	v_mul_f32_e32 v6, 0xbfb8aa3b, v6
	v_cndmask_b32_e32 v2, v7, v2, vcc
	v_mul_f32_e32 v4, 0xbfb8aa3b, v4
	v_exp_f32_e32 v5, v5
	v_exp_f32_e32 v7, v6
	v_and_b32_e32 v6, 0xffff0000, v45
	v_exp_f32_e32 v4, v4
	v_mul_f32_e32 v6, 0xbfb8aa3b, v6
	v_exp_f32_e32 v23, v6
	v_add_f32_e32 v5, 1.0, v5
	v_add_f32_e32 v4, 1.0, v4
	v_rcp_f32_e32 v6, v5
	v_add_f32_e32 v5, 1.0, v7
	v_rcp_f32_e32 v4, v4
	v_rcp_f32_e32 v5, v5
	v_add_f32_e32 v7, 1.0, v23
	v_rcp_f32_e32 v7, v7
	v_mov_b32_e32 v24, v8
	v_mov_b32_e32 v25, v10
	v_pk_mul_f32 v[4:5], v[4:5], v[24:25]
	v_mov_b32_e32 v10, v9
	v_pk_mul_f32 v[4:5], v[4:5], v[2:3] op_sel_hi:[1,0]
	v_pk_mul_f32 v[6:7], v[6:7], v[10:11]
	v_pk_mul_f32 v[4:5], v[14:15], v[4:5]
	v_pk_mul_f32 v[6:7], v[6:7], v[2:3] op_sel_hi:[1,0]
	v_and_b32_sdwa v8, v4, v113 dst_sel:DWORD dst_unused:UNUSED_PAD src0_sel:WORD_1 src1_sel:DWORD
	v_pk_mul_f32 v[6:7], v[38:39], v[6:7]
	v_add3_u32 v23, v4, v8, s20
	v_and_b32_sdwa v4, v7, v113 dst_sel:DWORD dst_unused:UNUSED_PAD src0_sel:WORD_1 src1_sel:DWORD
	v_and_b32_sdwa v2, v5, v113 dst_sel:DWORD dst_unused:UNUSED_PAD src0_sel:WORD_1 src1_sel:DWORD
	v_add3_u32 v4, v7, v4, s20
	s_or_b32 s0, s24, 6
	v_add3_u32 v2, v5, v2, s20
	v_and_b32_sdwa v5, v6, v113 dst_sel:DWORD dst_unused:UNUSED_PAD src0_sel:WORD_1 src1_sel:DWORD
	v_and_b32_e32 v4, 0xffff0000, v4
	s_lshl_b64 s[10:11], s[6:7], 12
	s_ashr_i32 s1, s0, 31
	v_add3_u32 v5, v6, v5, s20
	v_or_b32_sdwa v25, v4, v2 dst_sel:DWORD dst_unused:UNUSED_PAD src0_sel:DWORD src1_sel:WORD_1
	v_lshl_add_u32 v2, s0, 10, v21
	s_add_u32 s6, s0, s8
	v_and_b32_e32 v24, 0xffff0000, v5
	ds_read_b128 v[4:7], v2
	s_addc_u32 s7, s1, 0
	s_or_b32 s9, s24, 7
	v_lshl_add_u32 v2, s9, 10, v21
	ds_read_b128 v[8:11], v2
	s_waitcnt lgkmcnt(1)
	v_pk_mul_f32 v[26:27], v[6:7], v[6:7]
	v_pk_mul_f32 v[28:29], v[4:5], v[4:5]
	v_or_b32_sdwa v24, v24, v23 dst_sel:DWORD dst_unused:UNUSED_PAD src0_sel:DWORD src1_sel:WORD_1
	v_pk_mov_b32 v[30:31], v[28:29], v[26:27] op_sel:[1,0]
	v_mov_b32_e32 v29, v27
	v_pk_add_f32 v[26:27], v[30:31], v[28:29]
	s_waitcnt lgkmcnt(0)
	v_pk_mul_f32 v[28:29], v[10:11], v[10:11]
	v_pk_mul_f32 v[30:31], v[8:9], v[8:9]
	v_lshlrev_b32_e32 v2, 16, v42
	v_pk_mov_b32 v[32:33], v[30:31], v[28:29] op_sel:[1,0]
	v_mov_b32_e32 v31, v29
	v_pk_add_f32 v[28:29], v[32:33], v[30:31]
	v_mov_b32_e32 v31, v26
	v_mov_b32_e32 v30, v28
	v_mov_b32_e32 v26, v29
	v_pk_add_f32 v[26:27], v[30:31], v[26:27]
	ds_bpermute_b32 v21, v20, v27
	ds_bpermute_b32 v20, v20, v26
	v_lshl_add_u64 v[28:29], v[12:13], 0, s[10:11]
	global_store_dwordx2 v[28:29], v[24:25], off
	v_mul_f32_e32 v2, 0xbfb8aa3b, v2
	v_exp_f32_e32 v2, v2
	s_waitcnt lgkmcnt(0)
	v_pk_add_f32 v[20:21], v[26:27], v[20:21]
	ds_bpermute_b32 v25, v18, v21
	ds_bpermute_b32 v24, v18, v20
	v_add_f32_e32 v2, 1.0, v2
	v_rcp_f32_e32 v18, v2
	v_and_b32_e32 v2, 0xffff0000, v42
	v_mul_f32_e32 v2, 0xbfb8aa3b, v2
	s_waitcnt lgkmcnt(0)
	v_pk_add_f32 v[20:21], v[20:21], v[24:25]
	ds_bpermute_b32 v23, v22, v21
	ds_bpermute_b32 v22, v22, v20
	v_exp_f32_e32 v2, v2
	v_mov_b32_e32 v26, v4
	v_mov_b32_e32 v27, v6
	v_mov_b32_e32 v6, v5
	s_waitcnt lgkmcnt(0)
	v_pk_add_f32 v[20:21], v[20:21], v[22:23]
	ds_bpermute_b32 v23, v19, v21
	ds_bpermute_b32 v22, v19, v20
	v_add_f32_e32 v2, 1.0, v2
	v_rcp_f32_e32 v24, v2
	v_lshlrev_b32_e32 v2, 16, v43
	v_mul_f32_e32 v2, 0xbfb8aa3b, v2
	s_waitcnt lgkmcnt(0)
	v_pk_add_f32 v[20:21], v[20:21], v[22:23]
	ds_bpermute_b32 v23, v57, v21
	ds_bpermute_b32 v22, v57, v20
	v_and_b32_e32 v19, 0xffff0000, v43
	v_exp_f32_e32 v2, v2
	v_mul_f32_e32 v19, 0xbfb8aa3b, v19
	v_exp_f32_e32 v25, v19
	s_waitcnt lgkmcnt(0)
	v_pk_add_f32 v[20:21], v[20:21], v[22:23]
	ds_bpermute_b32 v23, v56, v21
	ds_bpermute_b32 v22, v56, v20
	v_add_f32_e32 v2, 1.0, v2
	v_rcp_f32_e32 v19, v2
	v_add_f32_e32 v2, 1.0, v25
	v_rcp_f32_e32 v25, v2
	s_waitcnt lgkmcnt(0)
	v_pk_add_f32 v[4:5], v[20:21], v[22:23]
	v_pk_mul_f32 v[18:19], v[18:19], v[26:27]
	v_pk_fma_f32 v[4:5], v[4:5], s[80:81], v[16:17] op_sel_hi:[1,0,0]
	v_pk_mul_f32 v[6:7], v[24:25], v[6:7]
	v_mul_f32_e32 v2, 0x4b800000, v5
	v_cmp_gt_f32_e32 vcc, s19, v5
	s_lshl_b64 s[6:7], s[6:7], 12
	v_lshl_add_u64 v[16:17], v[12:13], 0, s[6:7]
	v_cndmask_b32_e32 v2, v5, v2, vcc
	v_rsq_f32_e32 v2, v2
	s_ashr_i32 s0, s9, 31
	s_add_u32 s6, s9, s8
	s_addc_u32 s7, s0, 0
	v_mul_f32_e32 v5, 0x45800000, v2
	v_cndmask_b32_e32 v2, v2, v5, vcc
	v_pk_mul_f32 v[18:19], v[18:19], v[2:3] op_sel_hi:[1,0]
	v_pk_mul_f32 v[6:7], v[6:7], v[2:3] op_sel_hi:[1,0]
	v_pk_mul_f32 v[18:19], v[14:15], v[18:19]
	v_pk_mul_f32 v[6:7], v[38:39], v[6:7]
	v_and_b32_sdwa v5, v18, v113 dst_sel:DWORD dst_unused:UNUSED_PAD src0_sel:WORD_1 src1_sel:DWORD
	v_add3_u32 v18, v18, v5, s20
	v_and_b32_sdwa v5, v7, v113 dst_sel:DWORD dst_unused:UNUSED_PAD src0_sel:WORD_1 src1_sel:DWORD
	v_and_b32_sdwa v2, v19, v113 dst_sel:DWORD dst_unused:UNUSED_PAD src0_sel:WORD_1 src1_sel:DWORD
	v_add3_u32 v5, v7, v5, s20
	v_mul_f32_e32 v7, 0x4b800000, v4
	v_cmp_gt_f32_e32 vcc, s19, v4
	v_add3_u32 v2, v19, v2, s20
	v_and_b32_sdwa v19, v6, v113 dst_sel:DWORD dst_unused:UNUSED_PAD src0_sel:WORD_1 src1_sel:DWORD
	v_cndmask_b32_e32 v4, v4, v7, vcc
	v_add3_u32 v6, v6, v19, s20
	v_rsq_f32_e32 v7, v4
	v_and_b32_e32 v5, 0xffff0000, v5
	v_and_b32_e32 v6, 0xffff0000, v6
	v_or_b32_sdwa v5, v5, v2 dst_sel:DWORD dst_unused:UNUSED_PAD src0_sel:DWORD src1_sel:WORD_1
	v_or_b32_sdwa v4, v6, v18 dst_sel:DWORD dst_unused:UNUSED_PAD src0_sel:DWORD src1_sel:WORD_1
	global_store_dwordx2 v[16:17], v[4:5], off
	v_and_b32_e32 v5, 0xffff0000, v40
	v_lshlrev_b32_e32 v6, 16, v41
	v_mul_f32_e32 v2, 0x45800000, v7
	v_lshlrev_b32_e32 v4, 16, v40
	v_mul_f32_e32 v5, 0xbfb8aa3b, v5
	v_mul_f32_e32 v6, 0xbfb8aa3b, v6
	v_cndmask_b32_e32 v2, v7, v2, vcc
	v_mul_f32_e32 v4, 0xbfb8aa3b, v4
	v_exp_f32_e32 v5, v5
	v_exp_f32_e32 v7, v6
	v_and_b32_e32 v6, 0xffff0000, v41
	v_exp_f32_e32 v4, v4
	v_mul_f32_e32 v6, 0xbfb8aa3b, v6
	v_exp_f32_e32 v16, v6
	v_add_f32_e32 v5, 1.0, v5
	v_add_f32_e32 v4, 1.0, v4
	v_rcp_f32_e32 v6, v5
	v_add_f32_e32 v5, 1.0, v7
	v_rcp_f32_e32 v4, v4
	v_rcp_f32_e32 v5, v5
	v_add_f32_e32 v7, 1.0, v16
	v_rcp_f32_e32 v7, v7
	v_mov_b32_e32 v16, v8
	v_mov_b32_e32 v17, v10
	v_pk_mul_f32 v[4:5], v[4:5], v[16:17]
	v_mov_b32_e32 v10, v9
	v_pk_mul_f32 v[4:5], v[4:5], v[2:3] op_sel_hi:[1,0]
	v_pk_mul_f32 v[6:7], v[6:7], v[10:11]
	v_pk_mul_f32 v[4:5], v[14:15], v[4:5]
	v_pk_mul_f32 v[6:7], v[6:7], v[2:3] op_sel_hi:[1,0]
	v_and_b32_sdwa v2, v5, v113 dst_sel:DWORD dst_unused:UNUSED_PAD src0_sel:WORD_1 src1_sel:DWORD
	v_pk_mul_f32 v[6:7], v[38:39], v[6:7]
	v_and_b32_sdwa v8, v4, v113 dst_sel:DWORD dst_unused:UNUSED_PAD src0_sel:WORD_1 src1_sel:DWORD
	v_add3_u32 v4, v4, v8, s20
	v_add3_u32 v2, v5, v2, s20
	v_and_b32_sdwa v5, v7, v113 dst_sel:DWORD dst_unused:UNUSED_PAD src0_sel:WORD_1 src1_sel:DWORD
	v_and_b32_sdwa v8, v6, v113 dst_sel:DWORD dst_unused:UNUSED_PAD src0_sel:WORD_1 src1_sel:DWORD
	v_add3_u32 v5, v7, v5, s20
	v_add3_u32 v6, v6, v8, s20
	v_and_b32_e32 v5, 0xffff0000, v5
	v_and_b32_e32 v6, 0xffff0000, v6
	s_lshl_b64 s[6:7], s[6:7], 12
	v_or_b32_sdwa v5, v5, v2 dst_sel:DWORD dst_unused:UNUSED_PAD src0_sel:DWORD src1_sel:WORD_1
	v_or_b32_sdwa v4, v6, v4 dst_sel:DWORD dst_unused:UNUSED_PAD src0_sel:DWORD src1_sel:WORD_1
	v_lshl_add_u64 v[6:7], v[12:13], 0, s[6:7]
	global_store_dwordx2 v[6:7], v[4:5], off
	s_waitcnt lgkmcnt(0)
	s_barrier
	s_setprio 0
	s_cmp_gt_i32 s60, 6
	s_cbranch_scc1 .LBB0_1760
	s_mul_i32 s0, s92, s60
	s_add_i32 s24, s93, s0
	s_add_i32 s0, s24, s92
	v_mov_b32_e32 v2, s75
	v_min3_i32 v2, s0, v2, v115
	s_cmp_lg_u32 s60, 0
	v_readfirstlane_b32 s53, v2
	s_barrier
	s_cbranch_scc1 .LBB0_1498
	v_mov_b32_e32 v2, v0
	v_readlane_b32 s8, v249, 53
	v_lshlrev_b32_e32 v4, 2, v2
	v_ashrrev_i32_e32 v5, 31, v4
	v_readlane_b32 s9, v249, 54
	s_barrier
	s_nop 0
	v_lshl_add_u64 v[4:5], v[4:5], 2, s[8:9]
	v_add_co_u32_e32 v6, vcc, 0x2000, v4
	global_load_dwordx4 v[28:31], v[4:5], off
	s_nop 0
	v_addc_co_u32_e32 v7, vcc, 0, v5, vcc
	global_load_dwordx4 v[32:35], v[6:7], off
	v_add_co_u32_e32 v6, vcc, 0x4000, v4
	s_mov_b32 s0, 0x8000
	s_nop 0
	v_addc_co_u32_e32 v7, vcc, 0, v5, vcc
	global_load_dwordx4 v[24:27], v[6:7], off
	v_add_co_u32_e32 v6, vcc, 0x6000, v4
	v_lshl_add_u32 v36, v2, 4, 0
	s_nop 0
	v_addc_co_u32_e32 v7, vcc, 0, v5, vcc
	global_load_dwordx4 v[16:19], v[6:7], off
	v_add_co_u32_e32 v6, vcc, s0, v4
	v_readlane_b32 s0, v249, 50
	s_nop 0
	v_addc_co_u32_e32 v7, vcc, 0, v5, vcc
	v_add_co_u32_e32 v8, vcc, 0xa000, v4
	v_readlane_b32 s1, v249, 51
	s_nop 0
	v_addc_co_u32_e32 v9, vcc, 0, v5, vcc
	global_load_dwordx4 v[20:23], v[6:7], off
	global_load_dwordx4 v[12:15], v[8:9], off
	v_add_co_u32_e32 v10, vcc, 0xc000, v4
	v_readlane_b32 s10, v249, 55
	s_nop 0
	v_addc_co_u32_e32 v11, vcc, 0, v5, vcc
	v_add_co_u32_e32 v4, vcc, 0xe000, v4
	v_readlane_b32 s11, v249, 56
	s_nop 0
	v_addc_co_u32_e32 v5, vcc, 0, v5, vcc
	global_load_dwordx4 v[8:11], v[10:11], off
	s_nop 0
	global_load_dwordx4 v[4:7], v[4:5], off
	s_andn2_b64 vcc, exec, s[0:1]
	s_waitcnt vmcnt(7)
	v_mul_f32_e32 v37, 0xbfb8aa3b, v28
	v_mul_f32_e32 v38, 0xbfb8aa3b, v29
	v_mul_f32_e32 v39, 0xbfb8aa3b, v30
	v_mul_f32_e32 v40, 0xbfb8aa3b, v31
	v_exp_f32_e32 v37, v37
	v_exp_f32_e32 v38, v38
	v_exp_f32_e32 v39, v39
	v_exp_f32_e32 v40, v40
	s_waitcnt vmcnt(6)
	v_mul_f32_e32 v41, 0xbfb8aa3b, v32
	v_mul_f32_e32 v42, 0xbfb8aa3b, v33
	v_mul_f32_e32 v43, 0xbfb8aa3b, v34
	v_mul_f32_e32 v44, 0xbfb8aa3b, v35
	v_exp_f32_e32 v45, v41
	v_exp_f32_e32 v42, v42
	v_exp_f32_e32 v43, v43
	v_exp_f32_e32 v44, v44
	s_waitcnt vmcnt(5)
	v_mul_f32_e32 v41, 0xbfb8aa3b, v24
	v_mul_f32_e32 v46, 0xbfb8aa3b, v25
	v_exp_f32_e32 v48, v41
	v_exp_f32_e32 v49, v46
	v_add_f32_e32 v37, 1.0, v37
	v_add_f32_e32 v41, 1.0, v38
	v_add_f32_e32 v46, 1.0, v39
	v_add_f32_e32 v50, 1.0, v40
	v_rcp_f32_e32 v38, v37
	v_rcp_f32_e32 v39, v41
	v_rcp_f32_e32 v40, v46
	v_rcp_f32_e32 v41, v50
	v_add_f32_e32 v37, 1.0, v45
	v_add_f32_e32 v45, 1.0, v42
	v_add_f32_e32 v46, 1.0, v43
	v_add_f32_e32 v50, 1.0, v44
	v_rcp_f32_e32 v42, v37
	v_rcp_f32_e32 v43, v45
	v_rcp_f32_e32 v44, v46
	v_rcp_f32_e32 v45, v50
	v_pk_mul_f32 v[30:31], v[30:31], v[40:41]
	v_pk_mul_f32 v[28:29], v[28:29], v[38:39]
	ds_write_b128 v36, v[28:31]
	v_pk_mul_f32 v[30:31], v[34:35], v[44:45]
	v_pk_mul_f32 v[28:29], v[32:33], v[42:43]
	v_mul_f32_e32 v47, 0xbfb8aa3b, v26
	ds_write_b128 v36, v[28:31] offset:8192
	v_mul_f32_e32 v28, 0xbfb8aa3b, v27
	v_exp_f32_e32 v47, v47
	v_exp_f32_e32 v29, v28
	v_add_f32_e32 v37, 1.0, v48
	v_add_f32_e32 v30, 1.0, v49
	v_add_f32_e32 v28, 1.0, v47
	v_add_f32_e32 v29, 1.0, v29
	v_rcp_f32_e32 v46, v37
	v_rcp_f32_e32 v28, v28
	v_rcp_f32_e32 v29, v29
	v_rcp_f32_e32 v47, v30
	s_waitcnt vmcnt(4)
	v_mul_f32_e32 v30, 0xbfb8aa3b, v16
	v_exp_f32_e32 v30, v30
	v_pk_mul_f32 v[26:27], v[26:27], v[28:29]
	v_pk_mul_f32 v[24:25], v[24:25], v[46:47]
	ds_write_b128 v36, v[24:27] offset:16384
	v_mul_f32_e32 v25, 0xbfb8aa3b, v17
	v_mul_f32_e32 v26, 0xbfb8aa3b, v18
	v_mul_f32_e32 v27, 0xbfb8aa3b, v19
	v_exp_f32_e32 v25, v25
	v_exp_f32_e32 v26, v26
	v_exp_f32_e32 v27, v27
	v_add_f32_e32 v24, 1.0, v30
	v_add_f32_e32 v25, 1.0, v25
	v_add_f32_e32 v26, 1.0, v26
	v_add_f32_e32 v27, 1.0, v27
	v_rcp_f32_e32 v24, v24
	v_rcp_f32_e32 v26, v26
	v_rcp_f32_e32 v27, v27
	v_rcp_f32_e32 v25, v25
	s_waitcnt vmcnt(3)
	v_mul_f32_e32 v28, 0xbfb8aa3b, v20
	v_exp_f32_e32 v28, v28
	v_pk_mul_f32 v[18:19], v[18:19], v[26:27]
	v_pk_mul_f32 v[16:17], v[16:17], v[24:25]
	ds_write_b128 v36, v[16:19] offset:24576
	v_mul_f32_e32 v17, 0xbfb8aa3b, v21
	v_mul_f32_e32 v18, 0xbfb8aa3b, v22
	v_mul_f32_e32 v19, 0xbfb8aa3b, v23
	v_exp_f32_e32 v17, v17
	v_exp_f32_e32 v18, v18
	v_exp_f32_e32 v19, v19
	v_add_f32_e32 v16, 1.0, v28
	v_add_f32_e32 v17, 1.0, v17
	v_add_f32_e32 v18, 1.0, v18
	v_add_f32_e32 v19, 1.0, v19
	v_rcp_f32_e32 v16, v16
	v_rcp_f32_e32 v18, v18
	v_rcp_f32_e32 v19, v19
	v_rcp_f32_e32 v17, v17
	s_waitcnt vmcnt(2)
	v_mul_f32_e32 v24, 0xbfb8aa3b, v12
	v_exp_f32_e32 v24, v24
	v_pk_mul_f32 v[18:19], v[22:23], v[18:19]
	v_pk_mul_f32 v[16:17], v[20:21], v[16:17]
	ds_write_b128 v36, v[16:19] offset:32768
	v_mul_f32_e32 v17, 0xbfb8aa3b, v13
	v_mul_f32_e32 v18, 0xbfb8aa3b, v14
	v_mul_f32_e32 v19, 0xbfb8aa3b, v15
	v_exp_f32_e32 v17, v17
	v_exp_f32_e32 v18, v18
	v_exp_f32_e32 v19, v19
	v_add_f32_e32 v16, 1.0, v24
	v_add_f32_e32 v17, 1.0, v17
	v_add_f32_e32 v18, 1.0, v18
	v_add_f32_e32 v19, 1.0, v19
	v_rcp_f32_e32 v16, v16
	v_rcp_f32_e32 v18, v18
	v_rcp_f32_e32 v19, v19
	v_rcp_f32_e32 v17, v17
	s_waitcnt vmcnt(1)
	v_mul_f32_e32 v20, 0xbfb8aa3b, v8
	v_exp_f32_e32 v20, v20
	v_pk_mul_f32 v[14:15], v[14:15], v[18:19]
	v_pk_mul_f32 v[12:13], v[12:13], v[16:17]
	ds_write_b128 v36, v[12:15] offset:40960
	v_mul_f32_e32 v14, 0xbfb8aa3b, v10
	v_mul_f32_e32 v15, 0xbfb8aa3b, v11
	v_exp_f32_e32 v14, v14
	v_exp_f32_e32 v15, v15
	s_waitcnt vmcnt(0)
	v_mul_f32_e32 v16, 0xbfb8aa3b, v4
	v_exp_f32_e32 v16, v16
	v_add_f32_e32 v14, 1.0, v14
	v_add_f32_e32 v15, 1.0, v15
	v_rcp_f32_e32 v14, v14
	v_rcp_f32_e32 v15, v15
	v_mul_f32_e32 v13, 0xbfb8aa3b, v9
	v_mul_f32_e32 v17, 0xbfb8aa3b, v7
	v_exp_f32_e32 v13, v13
	v_pk_mul_f32 v[10:11], v[10:11], v[14:15]
	v_add_f32_e32 v14, 1.0, v16
	v_mul_f32_e32 v15, 0xbfb8aa3b, v5
	v_mul_f32_e32 v16, 0xbfb8aa3b, v6
	v_exp_f32_e32 v15, v15
	v_exp_f32_e32 v16, v16
	v_exp_f32_e32 v17, v17
	v_add_f32_e32 v12, 1.0, v20
	v_add_f32_e32 v13, 1.0, v13
	v_add_f32_e32 v15, 1.0, v15
	v_add_f32_e32 v16, 1.0, v16
	v_add_f32_e32 v17, 1.0, v17
	v_rcp_f32_e32 v12, v12
	v_rcp_f32_e32 v13, v13
	v_rcp_f32_e32 v14, v14
	v_rcp_f32_e32 v16, v16
	v_rcp_f32_e32 v17, v17
	v_rcp_f32_e32 v15, v15
	v_pk_mul_f32 v[8:9], v[8:9], v[12:13]
	ds_write_b128 v36, v[8:11] offset:49152
	v_pk_mul_f32 v[6:7], v[6:7], v[16:17]
	v_pk_mul_f32 v[4:5], v[4:5], v[14:15]
	ds_write_b128 v36, v[4:7] offset:57344
	s_waitcnt lgkmcnt(0)
	s_barrier
	s_cbranch_vccnz .LBB0_1498
	s_mov_b32 s0, 0x2aaaaaab
	v_mul_hi_i32 v6, v2, s0
	v_ashrrev_i32_e32 v4, 1, v6
	v_lshrrev_b32_e32 v7, 31, v6
	v_add_u32_e32 v121, v4, v7
	v_mul_lo_u32 v4, v121, 12
	v_sub_u32_e32 v4, v2, v4
	v_lshlrev_b32_e32 v4, 2, v4
	v_readlane_b32 s8, v249, 53
	v_ashrrev_i32_e32 v5, 31, v4
	v_readlane_b32 s10, v249, 55
	v_readlane_b32 s11, v249, 56
	s_movk_i32 s0, 0x1f8
	v_cmp_gt_i32_e32 vcc, s0, v2
	v_lshl_add_u64 v[64:65], v[4:5], 2, s[10:11]
	v_ashrrev_i32_e32 v5, 3, v6
	v_add_u32_e32 v5, v5, v7
	s_movk_i32 s0, 0x180
	v_mul_lo_u32 v6, v5, 48
	v_lshlrev_b32_e32 v4, 7, v2
	v_cmp_gt_i32_e64 s[6:7], s0, v2
	v_sub_u32_e32 v2, v2, v6
	v_lshlrev_b32_e32 v7, 5, v2
	s_movk_i32 s0, 0x3000
	v_and_b32_e32 v7, 0xffffff80, v7
	v_and_b32_e32 v6, 3, v2
	v_mul_lo_u32 v123, v5, s0
	v_lshl_add_u32 v5, v5, 4, v7
	v_readlane_b32 s9, v249, 54
	v_add_u32_e32 v125, 42, v121
	v_add_u32_e32 v127, 0x54, v121
	v_add_u32_e32 v129, 0x7e, v121
	v_add_u32_e32 v131, 0xa8, v121
	v_add_u32_e32 v133, 0xd2, v121
	v_add_u32_e32 v135, 0xfc, v121
	v_lshl_or_b32 v5, v6, 2, v5
	v_add_u32_e32 v4, 0, v4
	v_mad_i64_i32 v[66:67], s[8:9], v121, s95, 0
	v_mad_i64_i32 v[68:69], s[8:9], v125, s95, 0
	v_mad_i64_i32 v[70:71], s[8:9], v127, s95, 0
	v_mad_i64_i32 v[72:73], s[8:9], v129, s95, 0
	v_mad_i64_i32 v[74:75], s[8:9], v131, s95, 0
	v_mad_i64_i32 v[76:77], s[8:9], v133, s95, 0
	v_mad_i64_i32 v[78:79], s[8:9], v135, s95, 0
	v_add_u32_e32 v137, 0, v5
	v_add_u32_e32 v139, 0x10000, v4
	v_readlane_b32 s25, v249, 52
	s_branch .LBB0_1376

.LBB0_2471:
	s_or_b64 exec, exec, s[6:7]
	s_waitcnt lgkmcnt(0)
	v_lshl_add_u32 v51, v160, 4, s75
	v_add3_u32 v50, s76, v166, v134
	ds_read_b32 v54, v51 offset:57472
	ds_read2_b32 v[52:53], v50 offset1:32
	s_lshl_b32 s2, s2, 1
	v_readlane_b32 s3, v249, 61
	s_add_u32 s2, s3, s2
	v_readlane_b32 s3, v249, 36
	s_waitcnt lgkmcnt(0)
	v_fma_f32 v2, v2, v54, v52
	v_fmac_f32_e32 v53, v18, v54
	ds_write2_b32 v50, v2, v53 offset1:32
	ds_read_b32 v2, v51 offset:57476
	ds_read2_b32 v[52:53], v50 offset0:64 offset1:96
	s_addc_u32 s3, s3, 0
	s_waitcnt lgkmcnt(0)
	v_fma_f32 v3, v3, v2, v52
	v_fmac_f32_e32 v53, v19, v2
	ds_write2_b32 v50, v3, v53 offset0:64 offset1:96
	ds_read_b32 v18, v51 offset:57480
	ds_read2_b32 v[2:3], v50 offset0:128 offset1:160
	v_add_u32_e32 v19, 0x1000, v50
	s_waitcnt lgkmcnt(0)
	v_fma_f32 v2, v4, v18, v2
	v_fmac_f32_e32 v3, v20, v18
	ds_write2_b32 v50, v2, v3 offset0:128 offset1:160
	ds_read_b32 v4, v51 offset:57484
	ds_read2_b32 v[2:3], v50 offset0:192 offset1:224
	v_add_u32_e32 v18, 0x800, v50
	v_add_u32_e32 v20, 0x1800, v50
	s_waitcnt lgkmcnt(0)
	v_fma_f32 v2, v5, v4, v2
	v_fmac_f32_e32 v3, v21, v4
	ds_write2_b32 v50, v2, v3 offset0:192 offset1:224
	ds_read_b32 v4, v51 offset:57504
	ds_read2_b32 v[2:3], v18 offset1:32
	s_waitcnt lgkmcnt(0)
	v_fma_f32 v2, v6, v4, v2
	v_fmac_f32_e32 v3, v22, v4
	ds_write2_b32 v18, v2, v3 offset1:32
	ds_read_b32 v4, v51 offset:57508
	ds_read2_b32 v[2:3], v18 offset0:64 offset1:96
	s_waitcnt lgkmcnt(0)
	v_fma_f32 v2, v7, v4, v2
	v_fmac_f32_e32 v3, v23, v4
	ds_write2_b32 v18, v2, v3 offset0:64 offset1:96
	ds_read_b32 v4, v51 offset:57512
	ds_read2_b32 v[2:3], v18 offset0:128 offset1:160
	s_waitcnt lgkmcnt(0)
	v_fma_f32 v2, v8, v4, v2
	v_fmac_f32_e32 v3, v24, v4
	ds_write2_b32 v18, v2, v3 offset0:128 offset1:160
	ds_read_b32 v4, v51 offset:57516
	ds_read2_b32 v[2:3], v18 offset0:192 offset1:224
	s_waitcnt lgkmcnt(0)
	v_fma_f32 v2, v9, v4, v2
	v_fmac_f32_e32 v3, v25, v4
	ds_write2_b32 v18, v2, v3 offset0:192 offset1:224
	ds_read_b32 v4, v51 offset:57536
	ds_read2_b32 v[2:3], v19 offset1:32
	s_waitcnt lgkmcnt(0)
	v_fma_f32 v2, v10, v4, v2
	v_fmac_f32_e32 v3, v26, v4
	ds_write2_b32 v19, v2, v3 offset1:32
	ds_read_b32 v4, v51 offset:57540
	ds_read2_b32 v[2:3], v19 offset0:64 offset1:96
	s_waitcnt lgkmcnt(0)
	v_fma_f32 v2, v11, v4, v2
	v_fmac_f32_e32 v3, v27, v4
	ds_write2_b32 v19, v2, v3 offset0:64 offset1:96
	ds_read_b32 v4, v51 offset:57544
	ds_read2_b32 v[2:3], v19 offset0:128 offset1:160
	s_waitcnt lgkmcnt(0)
	v_fma_f32 v2, v12, v4, v2
	v_fmac_f32_e32 v3, v28, v4
	ds_write2_b32 v19, v2, v3 offset0:128 offset1:160
	ds_read_b32 v4, v51 offset:57548
	ds_read2_b32 v[2:3], v19 offset0:192 offset1:224
	s_waitcnt lgkmcnt(0)
	v_fma_f32 v2, v13, v4, v2
	v_fmac_f32_e32 v3, v29, v4
	ds_write2_b32 v19, v2, v3 offset0:192 offset1:224
	ds_read_b32 v4, v51 offset:57568
	ds_read2_b32 v[2:3], v20 offset1:32
	s_waitcnt lgkmcnt(0)
	v_fma_f32 v2, v14, v4, v2
	v_fmac_f32_e32 v3, v30, v4
	ds_write2_b32 v20, v2, v3 offset1:32
	ds_read_b32 v4, v51 offset:57572
	ds_read2_b32 v[2:3], v20 offset0:64 offset1:96
	s_waitcnt lgkmcnt(0)
	v_fma_f32 v2, v15, v4, v2
	v_fmac_f32_e32 v3, v31, v4
	ds_write2_b32 v20, v2, v3 offset0:64 offset1:96
	ds_read_b32 v4, v51 offset:57576
	ds_read2_b32 v[2:3], v20 offset0:128 offset1:160
	s_waitcnt lgkmcnt(0)
	v_fma_f32 v2, v16, v4, v2
	v_fmac_f32_e32 v3, v32, v4
	ds_write2_b32 v20, v2, v3 offset0:128 offset1:160
	ds_read_b32 v4, v51 offset:57580
	ds_read2_b32 v[2:3], v20 offset0:192 offset1:224
	s_waitcnt lgkmcnt(0)
	v_fma_f32 v2, v17, v4, v2
	v_fmac_f32_e32 v3, v33, v4
	ds_write2_b32 v20, v2, v3 offset0:192 offset1:224
	v_mov_b64_e32 v[2:3], v[66:67]
	s_waitcnt lgkmcnt(0)
	v_mov_b64_e32 v[4:5], v[68:69]
	v_mov_b64_e32 v[6:7], v[70:71]
	v_mov_b64_e32 v[8:9], v[72:73]
	v_mov_b64_e32 v[10:11], v[74:75]
	v_mov_b64_e32 v[12:13], v[76:77]
	v_mov_b64_e32 v[14:15], v[78:79]
	v_mov_b64_e32 v[16:17], v[80:81]
	ds_read2_b32 v[2:3], v50 offset1:32
	s_waitcnt vmcnt(31) lgkmcnt(0)
	v_add_f32_e32 v4, v96, v2
	s_waitcnt vmcnt(30)
	v_add_f32_e32 v5, v97, v3
	ds_read2_b32 v[2:3], v50 offset0:64 offset1:96
	s_waitcnt vmcnt(29) lgkmcnt(0)
	v_add_f32_e32 v6, v94, v2
	s_waitcnt vmcnt(28)
	v_add_f32_e32 v7, v95, v3
	ds_read2_b32 v[2:3], v50 offset0:128 offset1:160
	s_waitcnt vmcnt(27) lgkmcnt(0)
	v_add_f32_e32 v8, v92, v2
	s_waitcnt vmcnt(26)
	v_add_f32_e32 v9, v93, v3
	ds_read2_b32 v[2:3], v50 offset0:192 offset1:224
	s_waitcnt vmcnt(25) lgkmcnt(0)
	v_add_f32_e32 v10, v90, v2
	s_waitcnt vmcnt(24)
	v_add_f32_e32 v11, v91, v3
	ds_read2_b32 v[2:3], v18 offset1:32
	s_waitcnt vmcnt(23) lgkmcnt(0)
	v_add_f32_e32 v12, v86, v2
	s_waitcnt vmcnt(22)
	v_add_f32_e32 v13, v87, v3
	ds_read2_b32 v[2:3], v18 offset0:64 offset1:96
	s_waitcnt vmcnt(21) lgkmcnt(0)
	v_add_f32_e32 v14, v84, v2
	s_waitcnt vmcnt(20)
	v_add_f32_e32 v15, v85, v3
	ds_read2_b32 v[2:3], v18 offset0:128 offset1:160
	s_waitcnt vmcnt(19) lgkmcnt(0)
	v_add_f32_e32 v16, v82, v2
	s_waitcnt vmcnt(18)
	v_add_f32_e32 v17, v83, v3
	ds_read2_b32 v[2:3], v18 offset0:192 offset1:224
	s_waitcnt vmcnt(17) lgkmcnt(0)
	v_add_f32_e32 v18, v46, v2
	s_waitcnt vmcnt(16)
	v_add_f32_e32 v21, v47, v3
	ds_read2_b32 v[2:3], v19 offset1:32
	s_waitcnt vmcnt(15) lgkmcnt(0)
	v_add_f32_e32 v22, v58, v2
	s_waitcnt vmcnt(14)
	v_add_f32_e32 v23, v59, v3
	ds_read2_b32 v[2:3], v19 offset0:64 offset1:96
	s_waitcnt vmcnt(13) lgkmcnt(0)
	v_add_f32_e32 v24, v48, v2
	s_waitcnt vmcnt(12)
	v_add_f32_e32 v25, v49, v3
	ds_read2_b32 v[2:3], v19 offset0:128 offset1:160
	s_waitcnt vmcnt(11) lgkmcnt(0)
	v_add_f32_e32 v26, v44, v2
	s_waitcnt vmcnt(10)
	v_add_f32_e32 v27, v45, v3
	ds_read2_b32 v[2:3], v19 offset0:192 offset1:224
	s_waitcnt vmcnt(9) lgkmcnt(0)
	v_add_f32_e32 v19, v40, v2
	s_waitcnt vmcnt(8)
	v_add_f32_e32 v28, v41, v3
	ds_read2_b32 v[2:3], v20 offset1:32
	s_waitcnt vmcnt(7) lgkmcnt(0)
	v_add_f32_e32 v29, v42, v2
	s_waitcnt vmcnt(6)
	v_add_f32_e32 v30, v43, v3
	ds_read2_b32 v[2:3], v20 offset0:64 offset1:96
	s_waitcnt vmcnt(5) lgkmcnt(0)
	v_add_f32_e32 v31, v38, v2
	s_waitcnt vmcnt(4)
	v_add_f32_e32 v32, v39, v3
	ds_read2_b32 v[2:3], v20 offset0:128 offset1:160
	s_waitcnt vmcnt(3) lgkmcnt(0)
	v_add_f32_e32 v33, v36, v2
	s_waitcnt vmcnt(2)
	v_add_f32_e32 v36, v37, v3
	ds_read2_b32 v[2:3], v20 offset0:192 offset1:224
	v_lshlrev_b32_e32 v20, 9, v160
	s_waitcnt lgkmcnt(0)
	s_waitcnt vmcnt(1) lgkmcnt(0)
	v_add_f32_e32 v2, v34, v2
	v_lshlrev_b32_e32 v34, 1, v162
	v_add3_u32 v20, s76, v20, v34
	v_bfe_u32 v34, v4, 16, 1
	v_add3_u32 v4, v4, v34, s74
	ds_write_b16_d16_hi v20, v4
	v_bfe_u32 v4, v5, 16, 1
	v_add3_u32 v4, v5, v4, s74
	ds_write_b16_d16_hi v20, v4 offset:64
	v_bfe_u32 v4, v6, 16, 1
	v_add3_u32 v4, v6, v4, s74
	ds_write_b16_d16_hi v20, v4 offset:128
	v_bfe_u32 v4, v7, 16, 1
	v_add3_u32 v4, v7, v4, s74
	ds_write_b16_d16_hi v20, v4 offset:192
	v_bfe_u32 v4, v8, 16, 1
	v_add3_u32 v4, v8, v4, s74
	ds_write_b16_d16_hi v20, v4 offset:256
	v_bfe_u32 v4, v9, 16, 1
	v_add3_u32 v4, v9, v4, s74
	ds_write_b16_d16_hi v20, v4 offset:320
	v_bfe_u32 v4, v10, 16, 1
	v_add3_u32 v4, v10, v4, s74
	ds_write_b16_d16_hi v20, v4 offset:384
	v_bfe_u32 v4, v11, 16, 1
	v_add3_u32 v4, v11, v4, s74
	ds_write_b16_d16_hi v20, v4 offset:448
	v_bfe_u32 v4, v12, 16, 1
	v_add3_u32 v4, v12, v4, s74
	ds_write_b16_d16_hi v20, v4 offset:1024
	v_bfe_u32 v4, v13, 16, 1
	v_add3_u32 v4, v13, v4, s74
	ds_write_b16_d16_hi v20, v4 offset:1088
	v_bfe_u32 v4, v14, 16, 1
	v_add3_u32 v4, v14, v4, s74
	ds_write_b16_d16_hi v20, v4 offset:1152
	v_bfe_u32 v4, v15, 16, 1
	v_add3_u32 v4, v15, v4, s74
	ds_write_b16_d16_hi v20, v4 offset:1216
	v_bfe_u32 v4, v16, 16, 1
	v_add3_u32 v4, v16, v4, s74
	ds_write_b16_d16_hi v20, v4 offset:1280
	v_bfe_u32 v4, v17, 16, 1
	v_add3_u32 v4, v17, v4, s74
	ds_write_b16_d16_hi v20, v4 offset:1344
	v_bfe_u32 v4, v18, 16, 1
	v_add3_u32 v4, v18, v4, s74
	ds_write_b16_d16_hi v20, v4 offset:1408
	v_bfe_u32 v4, v21, 16, 1
	v_add3_u32 v4, v21, v4, s74
	ds_write_b16_d16_hi v20, v4 offset:1472
	v_bfe_u32 v4, v22, 16, 1
	v_add3_u32 v4, v22, v4, s74
	ds_write_b16_d16_hi v20, v4 offset:2048
	v_bfe_u32 v4, v23, 16, 1
	v_add3_u32 v4, v23, v4, s74
	ds_write_b16_d16_hi v20, v4 offset:2112
	v_bfe_u32 v4, v24, 16, 1
	v_add3_u32 v4, v24, v4, s74
	ds_write_b16_d16_hi v20, v4 offset:2176
	v_bfe_u32 v4, v25, 16, 1
	v_add3_u32 v4, v25, v4, s74
	ds_write_b16_d16_hi v20, v4 offset:2240
	v_bfe_u32 v4, v26, 16, 1
	v_add3_u32 v4, v26, v4, s74
	ds_write_b16_d16_hi v20, v4 offset:2304
	v_bfe_u32 v4, v27, 16, 1
	v_add3_u32 v4, v27, v4, s74
	ds_write_b16_d16_hi v20, v4 offset:2368
	v_bfe_u32 v4, v19, 16, 1
	v_add3_u32 v4, v19, v4, s74
	ds_write_b16_d16_hi v20, v4 offset:2432
	v_bfe_u32 v4, v28, 16, 1
	v_add3_u32 v4, v28, v4, s74
	ds_write_b16_d16_hi v20, v4 offset:2496
	v_bfe_u32 v4, v29, 16, 1
	v_add3_u32 v4, v29, v4, s74
	ds_write_b16_d16_hi v20, v4 offset:3072
	v_bfe_u32 v4, v30, 16, 1
	v_add3_u32 v4, v30, v4, s74
	ds_write_b16_d16_hi v20, v4 offset:3136
	v_bfe_u32 v4, v31, 16, 1
	v_add3_u32 v4, v31, v4, s74
	ds_write_b16_d16_hi v20, v4 offset:3200
	v_bfe_u32 v4, v32, 16, 1
	v_add3_u32 v4, v32, v4, s74
	ds_write_b16_d16_hi v20, v4 offset:3264
	v_bfe_u32 v4, v33, 16, 1
	v_add3_u32 v4, v33, v4, s74
	ds_write_b16_d16_hi v20, v4 offset:3328
	v_bfe_u32 v4, v36, 16, 1
	v_add3_u32 v4, v36, v4, s74
	ds_write_b16_d16_hi v20, v4 offset:3392
	v_bfe_u32 v4, v2, 16, 1
	s_waitcnt vmcnt(0)
	v_add_f32_e32 v3, v35, v3
	v_add3_u32 v2, v2, v4, s74
	ds_write_b16_d16_hi v20, v2 offset:3456
	v_bfe_u32 v2, v3, 16, 1
	v_add3_u32 v2, v3, v2, s74
	ds_write_b16_d16_hi v20, v2 offset:3520
	v_lshlrev_b32_e32 v2, 1, v158
	v_and_b32_e32 v130, 0x70, v2
	s_waitcnt lgkmcnt(0)
	v_lshrrev_b32_e32 v12, 3, v137
	v_add_u32_e32 v13, s76, v130
	v_lshl_add_u32 v2, v12, 7, v13
	ds_read_b128 v[2:5], v2
	v_or_b32_e32 v8, s0, v12
	v_mov_b32_e32 v9, s1
	v_lshl_add_u64 v[6:7], s[2:3], 0, v[130:131]
	v_lshlrev_b64 v[10:11], 12, v[8:9]
	v_lshl_add_u64 v[10:11], v[6:7], 0, v[10:11]
	v_or_b32_e32 v8, 8, v12
	s_waitcnt lgkmcnt(0)
	global_store_dwordx4 v[10:11], v[2:5], off
	s_nop 1
	v_lshl_add_u32 v2, v8, 7, v13
	ds_read_b128 v[2:5], v2
	v_or_b32_e32 v8, s0, v8
	v_lshlrev_b64 v[10:11], 12, v[8:9]
	v_lshl_add_u64 v[10:11], v[6:7], 0, v[10:11]
	v_or_b32_e32 v8, 16, v12
	s_waitcnt lgkmcnt(0)
	global_store_dwordx4 v[10:11], v[2:5], off
	s_nop 1
	v_lshl_add_u32 v2, v8, 7, v13
	ds_read_b128 v[2:5], v2
	v_or_b32_e32 v8, s0, v8
	v_lshlrev_b64 v[10:11], 12, v[8:9]
	v_lshl_add_u64 v[10:11], v[6:7], 0, v[10:11]
	v_or_b32_e32 v8, 24, v12
	s_waitcnt lgkmcnt(0)
	global_store_dwordx4 v[10:11], v[2:5], off
	s_nop 1
	v_lshl_add_u32 v2, v8, 7, v13
	ds_read_b128 v[2:5], v2
	v_or_b32_e32 v8, s0, v8
	v_lshlrev_b64 v[8:9], 12, v[8:9]
	v_lshl_add_u64 v[6:7], v[6:7], 0, v[8:9]
	s_waitcnt lgkmcnt(0)
	global_store_dwordx4 v[6:7], v[2:5], off
	s_waitcnt lgkmcnt(0)
	s_barrier
	s_setprio 0
	v_readlane_b32 s42, v249, 26
	v_readlane_b32 s50, v249, 30
	s_cmp_gt_i32 s60, 6
	v_readlane_b32 s43, v249, 27
	v_readlane_b32 s51, v249, 31
	s_cbranch_scc1 .LBB0_2336
	s_mul_i32 s0, s60, 48
	v_readlane_b32 s1, v248, 47
	s_add_i32 s6, s1, s0
	v_readlane_b32 s1, v248, 48
	s_add_i32 s0, s6, 48
	s_cmp_lg_u32 s60, 0
	v_mov_b32_e32 v2, s1
	v_min3_i32 v2, s0, v2, v165
	s_nop 0
	v_readfirstlane_b32 s26, v2
	s_barrier
	s_cbranch_scc1 .LBB0_2595
	v_mov_b32_e32 v109, v0
	v_readlane_b32 s0, v248, 56
	v_lshlrev_b32_e32 v2, 2, v109
	v_ashrrev_i32_e32 v3, 31, v2
	v_readlane_b32 s1, v248, 57
	s_barrier
	s_nop 0
	v_lshl_add_u64 v[2:3], v[2:3], 2, s[0:1]
	global_load_dwordx4 v[32:35], v[2:3], off
	v_add_co_u32_e32 v4, vcc, 0x2000, v2
	s_movk_i32 s0, 0x4000
	s_nop 0
	v_addc_co_u32_e32 v5, vcc, 0, v3, vcc
	global_load_dwordx4 v[26:29], v[4:5], off
	v_add_co_u32_e32 v4, vcc, s0, v2
	v_lshl_add_u32 v30, v109, 4, 0
	s_nop 0
	v_addc_co_u32_e32 v5, vcc, 0, v3, vcc
	global_load_dwordx4 v[22:25], v[4:5], off
	v_add_co_u32_e32 v4, vcc, 0x6000, v2
	v_readlane_b32 s0, v248, 49
	s_nop 0
	v_addc_co_u32_e32 v5, vcc, 0, v3, vcc
	global_load_dwordx4 v[18:21], v[4:5], off
	v_add_co_u32_e32 v4, vcc, 0x8000, v2
	v_readlane_b32 s1, v248, 50
	s_nop 0
	v_addc_co_u32_e32 v5, vcc, 0, v3, vcc
	global_load_dwordx4 v[14:17], v[4:5], off
	v_add_co_u32_e32 v4, vcc, 0xa000, v2
	v_readlane_b32 s2, v248, 58
	s_nop 0
	v_addc_co_u32_e32 v5, vcc, 0, v3, vcc
	global_load_dwordx4 v[10:13], v[4:5], off
	v_add_co_u32_e32 v4, vcc, 0xc000, v2
	v_readlane_b32 s3, v248, 59
	s_nop 0
	v_addc_co_u32_e32 v5, vcc, 0, v3, vcc
	global_load_dwordx4 v[6:9], v[4:5], off
	v_add_co_u32_e32 v2, vcc, 0xe000, v2
	s_waitcnt vmcnt(6)
	v_mul_f32_e32 v31, 0xbfb8aa3b, v32
	v_exp_f32_e32 v31, v31
	v_addc_co_u32_e32 v3, vcc, 0, v3, vcc
	global_load_dwordx4 v[2:5], v[2:3], off
	v_add_f32_e32 v31, 1.0, v31
	v_rcp_f32_e32 v36, v31
	v_mul_f32_e32 v31, 0xbfb8aa3b, v33
	v_exp_f32_e32 v31, v31
	s_andn2_b64 vcc, exec, s[0:1]
	v_add_f32_e32 v31, 1.0, v31
	v_rcp_f32_e32 v37, v31
	v_mul_f32_e32 v31, 0xbfb8aa3b, v34
	v_exp_f32_e32 v31, v31
	v_pk_mul_f32 v[32:33], v[32:33], v[36:37]
	v_add_f32_e32 v31, 1.0, v31
	v_rcp_f32_e32 v38, v31
	v_mul_f32_e32 v31, 0xbfb8aa3b, v35
	v_exp_f32_e32 v31, v31
	s_nop 0
	v_add_f32_e32 v31, 1.0, v31
	v_rcp_f32_e32 v39, v31
	s_waitcnt vmcnt(6)
	v_mul_f32_e32 v31, 0xbfb8aa3b, v26
	v_exp_f32_e32 v31, v31
	v_pk_mul_f32 v[34:35], v[34:35], v[38:39]
	ds_write_b128 v30, v[32:35]
	v_add_f32_e32 v31, 1.0, v31
	v_rcp_f32_e32 v32, v31
	v_mul_f32_e32 v31, 0xbfb8aa3b, v27
	v_exp_f32_e32 v31, v31
	s_nop 0
	v_add_f32_e32 v31, 1.0, v31
	v_rcp_f32_e32 v33, v31
	v_mul_f32_e32 v31, 0xbfb8aa3b, v28
	v_exp_f32_e32 v31, v31
	v_pk_mul_f32 v[26:27], v[26:27], v[32:33]
	v_add_f32_e32 v31, 1.0, v31
	v_rcp_f32_e32 v34, v31
	v_mul_f32_e32 v31, 0xbfb8aa3b, v29
	v_exp_f32_e32 v31, v31
	s_nop 0
	v_add_f32_e32 v31, 1.0, v31
	v_rcp_f32_e32 v35, v31
	s_nop 0
	v_pk_mul_f32 v[28:29], v[28:29], v[34:35]
	ds_write_b128 v30, v[26:29] offset:8192
	s_waitcnt vmcnt(5)
	v_mul_f32_e32 v26, 0xbfb8aa3b, v22
	v_mul_f32_e32 v27, 0xbfb8aa3b, v23
	v_mul_f32_e32 v28, 0xbfb8aa3b, v24
	v_mul_f32_e32 v29, 0xbfb8aa3b, v25
	v_exp_f32_e32 v26, v26
	v_exp_f32_e32 v27, v27
	v_exp_f32_e32 v28, v28
	v_exp_f32_e32 v29, v29
	v_add_f32_e32 v26, 1.0, v26
	v_add_f32_e32 v27, 1.0, v27
	v_add_f32_e32 v28, 1.0, v28
	v_add_f32_e32 v29, 1.0, v29
	v_rcp_f32_e32 v26, v26
	v_rcp_f32_e32 v27, v27
	v_rcp_f32_e32 v28, v28
	v_rcp_f32_e32 v29, v29
	v_pk_mul_f32 v[22:23], v[22:23], v[26:27]
	v_pk_mul_f32 v[24:25], v[24:25], v[28:29]
	ds_write_b128 v30, v[22:25] offset:16384
	s_waitcnt vmcnt(4)
	v_mul_f32_e32 v22, 0xbfb8aa3b, v18
	v_mul_f32_e32 v23, 0xbfb8aa3b, v19
	v_mul_f32_e32 v24, 0xbfb8aa3b, v20
	v_mul_f32_e32 v25, 0xbfb8aa3b, v21
	v_exp_f32_e32 v22, v22
	v_exp_f32_e32 v23, v23
	v_exp_f32_e32 v24, v24
	v_exp_f32_e32 v25, v25
	v_add_f32_e32 v22, 1.0, v22
	v_add_f32_e32 v23, 1.0, v23
	v_add_f32_e32 v24, 1.0, v24
	v_add_f32_e32 v25, 1.0, v25
	v_rcp_f32_e32 v22, v22
	v_rcp_f32_e32 v23, v23
	v_rcp_f32_e32 v24, v24
	v_rcp_f32_e32 v25, v25
	v_pk_mul_f32 v[18:19], v[18:19], v[22:23]
	v_pk_mul_f32 v[20:21], v[20:21], v[24:25]
	ds_write_b128 v30, v[18:21] offset:24576
	s_waitcnt vmcnt(3)
	v_mul_f32_e32 v18, 0xbfb8aa3b, v14
	v_mul_f32_e32 v19, 0xbfb8aa3b, v15
	v_mul_f32_e32 v20, 0xbfb8aa3b, v16
	v_mul_f32_e32 v21, 0xbfb8aa3b, v17
	v_exp_f32_e32 v18, v18
	v_exp_f32_e32 v19, v19
	v_exp_f32_e32 v20, v20
	v_exp_f32_e32 v21, v21
	v_add_f32_e32 v18, 1.0, v18
	v_add_f32_e32 v19, 1.0, v19
	v_add_f32_e32 v20, 1.0, v20
	v_add_f32_e32 v21, 1.0, v21
	v_rcp_f32_e32 v18, v18
	v_rcp_f32_e32 v19, v19
	v_rcp_f32_e32 v20, v20
	v_rcp_f32_e32 v21, v21
	v_pk_mul_f32 v[14:15], v[14:15], v[18:19]
	v_pk_mul_f32 v[16:17], v[16:17], v[20:21]
	ds_write_b128 v30, v[14:17] offset:32768
	s_waitcnt vmcnt(2)
	v_mul_f32_e32 v14, 0xbfb8aa3b, v10
	v_mul_f32_e32 v15, 0xbfb8aa3b, v11
	v_mul_f32_e32 v16, 0xbfb8aa3b, v12
	v_mul_f32_e32 v17, 0xbfb8aa3b, v13
	v_exp_f32_e32 v14, v14
	v_exp_f32_e32 v15, v15
	v_exp_f32_e32 v16, v16
	v_exp_f32_e32 v17, v17
	v_add_f32_e32 v14, 1.0, v14
	v_add_f32_e32 v15, 1.0, v15
	v_add_f32_e32 v16, 1.0, v16
	v_add_f32_e32 v17, 1.0, v17
	v_rcp_f32_e32 v14, v14
	v_rcp_f32_e32 v15, v15
	v_rcp_f32_e32 v16, v16
	v_rcp_f32_e32 v17, v17
	v_pk_mul_f32 v[10:11], v[10:11], v[14:15]
	v_pk_mul_f32 v[12:13], v[12:13], v[16:17]
	ds_write_b128 v30, v[10:13] offset:40960
	s_waitcnt vmcnt(1)
	v_mul_f32_e32 v10, 0xbfb8aa3b, v6
	v_mul_f32_e32 v11, 0xbfb8aa3b, v7
	v_mul_f32_e32 v12, 0xbfb8aa3b, v8
	v_mul_f32_e32 v13, 0xbfb8aa3b, v9
	v_exp_f32_e32 v10, v10
	v_exp_f32_e32 v11, v11
	v_exp_f32_e32 v12, v12
	v_exp_f32_e32 v13, v13
	v_add_f32_e32 v10, 1.0, v10
	v_add_f32_e32 v11, 1.0, v11
	v_add_f32_e32 v12, 1.0, v12
	v_add_f32_e32 v13, 1.0, v13
	v_rcp_f32_e32 v10, v10
	v_rcp_f32_e32 v11, v11
	v_rcp_f32_e32 v12, v12
	v_rcp_f32_e32 v13, v13
	v_pk_mul_f32 v[6:7], v[6:7], v[10:11]
	v_pk_mul_f32 v[8:9], v[8:9], v[12:13]
	ds_write_b128 v30, v[6:9] offset:49152
	s_waitcnt vmcnt(0)
	v_mul_f32_e32 v6, 0xbfb8aa3b, v2
	v_mul_f32_e32 v7, 0xbfb8aa3b, v3
	v_mul_f32_e32 v8, 0xbfb8aa3b, v4
	v_mul_f32_e32 v9, 0xbfb8aa3b, v5
	v_exp_f32_e32 v6, v6
	v_exp_f32_e32 v7, v7
	v_exp_f32_e32 v8, v8
	v_exp_f32_e32 v9, v9
	v_add_f32_e32 v6, 1.0, v6
	v_add_f32_e32 v7, 1.0, v7
	v_add_f32_e32 v8, 1.0, v8
	v_add_f32_e32 v9, 1.0, v9
	v_rcp_f32_e32 v6, v6
	v_rcp_f32_e32 v7, v7
	v_rcp_f32_e32 v8, v8
	v_rcp_f32_e32 v9, v9
	v_pk_mul_f32 v[2:3], v[2:3], v[6:7]
	v_pk_mul_f32 v[4:5], v[4:5], v[8:9]
	ds_write_b128 v30, v[2:5] offset:57344
	s_waitcnt lgkmcnt(0)
	s_barrier
	s_cbranch_vccnz .LBB0_2595
	s_movk_i32 s0, 0x1f8
	v_cmp_gt_i32_e32 vcc, s0, v109
	s_mov_b32 s0, 0x2aaaaaab
	v_mul_hi_i32 v111, v109, s0
	v_lshrrev_b32_e32 v113, 31, v111
	s_and_saveexec_b64 s[0:1], vcc
	s_cbranch_execz .LBB0_2592
	v_ashrrev_i32_e32 v2, 1, v111
	v_add_u32_e32 v115, v2, v113
	v_mul_lo_u32 v2, v115, 12
	v_sub_u32_e32 v2, v109, v2
	v_lshlrev_b32_e32 v2, 2, v2
	v_readlane_b32 s2, v248, 60
	v_ashrrev_i32_e32 v3, 31, v2
	v_readlane_b32 s3, v248, 61
	s_mov_b32 s4, 0xc000
	v_add_u32_e32 v117, 42, v115
	v_lshl_add_u64 v[62:63], v[2:3], 2, s[2:3]
	v_add_u32_e32 v119, 0x54, v115
	v_add_u32_e32 v121, 0x7e, v115
	v_add_u32_e32 v123, 0xa8, v115
	v_add_u32_e32 v125, 0xd2, v115
	v_add_u32_e32 v127, 0xfc, v115
	v_mad_i64_i32 v[2:3], s[2:3], v115, s4, v[62:63]
	v_mad_i64_i32 v[6:7], s[2:3], v117, s4, v[62:63]
	v_mad_i64_i32 v[10:11], s[2:3], v119, s4, v[62:63]
	v_mad_i64_i32 v[14:15], s[2:3], v121, s4, v[62:63]
	v_mad_i64_i32 v[18:19], s[2:3], v123, s4, v[62:63]
	v_mad_i64_i32 v[22:23], s[2:3], v125, s4, v[62:63]
	v_mad_i64_i32 v[26:27], s[2:3], v127, s4, v[62:63]
	global_load_dwordx4 v[2:5], v[2:3], off nt
	v_mov_b32_e32 v30, 0
	global_load_dwordx4 v[6:9], v[6:7], off nt
	s_mov_b32 s2, 0
	global_load_dwordx4 v[10:13], v[10:11], off nt
	v_mov_b32_e32 v31, v30
	global_load_dwordx4 v[14:17], v[14:15], off nt
	v_mov_b32_e32 v32, v30
	global_load_dwordx4 v[18:21], v[18:19], off nt
	v_mov_b32_e32 v33, v30
	global_load_dwordx4 v[22:25], v[22:23], off nt
	v_mov_b32_e32 v54, v30
	global_load_dwordx4 v[26:29], v[26:27], off nt
	v_mov_b32_e32 v55, v30
	v_mov_b32_e32 v56, v30
	v_mov_b32_e32 v57, v30
	v_mov_b32_e32 v50, v30
	v_mov_b32_e32 v51, v30
	v_mov_b32_e32 v52, v30
	v_mov_b32_e32 v53, v30
	v_mov_b32_e32 v46, v30
	v_mov_b32_e32 v47, v30
	v_mov_b32_e32 v48, v30
	v_mov_b32_e32 v49, v30
	v_mov_b32_e32 v42, v30
	v_mov_b32_e32 v43, v30
	v_mov_b32_e32 v44, v30
	v_mov_b32_e32 v45, v30
	v_mov_b32_e32 v38, v30
	v_mov_b32_e32 v39, v30
	v_mov_b32_e32 v40, v30
	v_mov_b32_e32 v41, v30
	v_mov_b32_e32 v34, v30
	v_mov_b32_e32 v35, v30
	v_mov_b32_e32 v36, v30
	v_mov_b32_e32 v37, v30
	v_mov_b32_e32 v58, v30
	v_mov_b32_e32 v59, v30
	v_mov_b32_e32 v60, v30
	v_mov_b32_e32 v61, v30
	s_waitcnt vmcnt(6)
	v_mov_b32_e32 v64, v2
	v_mov_b32_e32 v65, v3
	v_mov_b32_e32 v82, v4
	v_mov_b32_e32 v83, v5
	s_waitcnt vmcnt(5)
	v_mov_b32_e32 v84, v6
	v_mov_b32_e32 v85, v7
	v_mov_b32_e32 v86, v8
	v_mov_b32_e32 v87, v9
	s_waitcnt vmcnt(4)
	v_mov_b32_e32 v88, v10
	v_mov_b32_e32 v89, v11
	v_mov_b32_e32 v90, v12
	v_mov_b32_e32 v91, v13
	s_waitcnt vmcnt(3)
	v_mov_b32_e32 v92, v14
	v_mov_b32_e32 v93, v15
	v_mov_b32_e32 v94, v16
	v_mov_b32_e32 v95, v17
	s_waitcnt vmcnt(2)
	v_mov_b32_e32 v96, v18
	v_mov_b32_e32 v97, v19
	v_mov_b32_e32 v98, v20
	v_mov_b32_e32 v99, v21
	s_waitcnt vmcnt(1)
	v_mov_b32_e32 v100, v22
	v_mov_b32_e32 v101, v23
	v_mov_b32_e32 v102, v24
	v_mov_b32_e32 v103, v25
	s_waitcnt vmcnt(0)
	v_mov_b32_e32 v104, v26
	v_mov_b32_e32 v105, v27
	v_mov_b32_e32 v106, v28
	v_mov_b32_e32 v107, v29
	s_branch .LBB0_2477

.LBB0_2855:
	s_cmp_gt_i32 s64, 6
	s_cbranch_scc1 .LBB0_3243
	s_abs_i32 s4, s81
	v_cvt_f32_u32_e32 v1, s4
	s_sub_i32 s2, 0, s4
	s_add_i32 s0, s81, 0x17fff
	s_ashr_i32 s1, s0, 31
	v_rcp_iflag_f32_e32 v1, v1
	s_abs_i32 s0, s0
	s_ashr_i32 s5, s81, 31
	s_xor_b32 s1, s1, s5
	v_mul_f32_e32 v1, 0x4f7ffffe, v1
	v_cvt_u32_f32_e32 v1, v1
	v_readlane_b32 s10, v249, 1
	v_readlane_b32 s11, v249, 2
	v_mov_b32_e32 v113, 0x1be90
	v_readfirstlane_b32 s3, v1
	s_mul_i32 s2, s2, s3
	s_mul_hi_u32 s2, s3, s2
	s_add_i32 s6, s3, s2
	s_mul_hi_u32 s2, s0, s6
	s_mul_i32 s3, s2, s4
	s_sub_i32 s0, s0, s3
	s_add_i32 s7, s2, 1
	s_sub_i32 s3, s0, s4
	s_cmp_ge_u32 s0, s4
	s_cselect_b32 s2, s7, s2
	s_cselect_b32 s0, s3, s0
	s_add_i32 s3, s2, 1
	s_cmp_ge_u32 s0, s4
	s_cselect_b32 s0, s3, s2
	s_xor_b32 s0, s0, s1
	s_sub_i32 s0, s0, s1
	s_add_i32 s1, s0, 7
	s_ashr_i32 s2, s1, 31
	s_mul_i32 s3, s0, s87
	s_lshr_b32 s2, s2, 29
	s_add_i32 s1, s1, s2
	s_addk_i32 s3, 0x3e90
	s_ashr_i32 s2, s1, 3
	s_add_i32 s7, s3, s0
	s_load_dwordx4 s[16:19], s[10:11], 0x8
	s_load_dwordx2 s[0:1], s[10:11], 0x30
	s_load_dwordx4 s[12:15], s[10:11], 0x40
	s_add_i32 s8, s81, 0xa9
	s_load_dwordx4 s[20:23], s[10:11], 0xc8
	s_load_dwordx2 s[44:45], s[10:11], 0x80
	s_load_dwordx4 s[28:31], s[10:11], 0x70
	v_mov_b32_e32 v1, s7
	s_waitcnt lgkmcnt(0)
	v_writelane_b32 v249, s12, 20
	s_mov_b32 s90, 0xc000
	s_movk_i32 s91, 0x800
	v_writelane_b32 v249, s13, 21
	v_writelane_b32 v249, s14, 22
	v_writelane_b32 v249, s15, 23
	s_load_dwordx4 s[12:15], s[10:11], 0xd8
	v_readlane_b32 s9, v249, 16
	s_waitcnt lgkmcnt(0)
	s_load_dwordx2 s[12:13], s[10:11], 0x98
	v_mov_b32_e32 v67, 0
	s_movk_i32 s92, 0xc00
	s_add_u32 s34, s14, 0x100000
	s_addc_u32 s35, s15, 0
	s_lshl_b32 s9, s9, 14
	s_add_i32 s33, s9, 0
	s_add_u32 s9, s14, 0x1b000000
	v_writelane_b32 v249, s9, 52
	s_addc_u32 s9, s15, 0
	v_writelane_b32 v248, s9, 5
	s_add_u32 s9, s14, 0x2000000
	v_writelane_b32 v249, s9, 61
	s_addc_u32 s9, s15, 0
	v_writelane_b32 v249, s9, 36
	v_writelane_b32 v249, s20, 42
	s_add_u32 s9, s14, 0xb200000
	v_writelane_b32 v248, s9, 13
	v_writelane_b32 v249, s21, 43
	v_writelane_b32 v249, s22, 44
	v_writelane_b32 v249, s23, 45
	s_load_dwordx8 s[20:27], s[10:11], 0xa8
	s_addc_u32 s9, s15, 0
	s_movk_i32 s93, 0x3ff
	s_movk_i32 s94, 0xa2f
	s_movk_i32 s95, 0xe2f
	s_waitcnt lgkmcnt(0)
	v_writelane_b32 v249, s20, 53
	s_movk_i32 s36, 0x122f
	s_movk_i32 s37, 0x1237
	v_writelane_b32 v249, s21, 54
	v_writelane_b32 v249, s22, 55
	v_writelane_b32 v249, s23, 56
	v_writelane_b32 v249, s24, 57
	v_writelane_b32 v249, s25, 58
	v_writelane_b32 v249, s26, 59
	v_writelane_b32 v249, s27, 60
	v_writelane_b32 v249, s9, 38
	s_add_u32 s9, s14, 0xb500000
	v_writelane_b32 v249, s9, 40
	s_addc_u32 s9, s15, 0
	s_add_u32 s38, s14, 0xb400000
	s_addc_u32 s39, s15, 0
	s_add_u32 s40, s14, 0x6000000
	s_addc_u32 s41, s15, 0
	s_add_u32 s42, s14, 0x23000000
	s_addc_u32 s43, s15, 0
	s_add_u32 s46, s14, 0xa200000
	s_addc_u32 s47, s15, 0
	s_add_u32 s48, s14, 0xaa00800
	s_addc_u32 s49, s15, 0
	s_add_u32 s50, s14, 0xaa00000
	s_addc_u32 s51, s15, 0
	s_add_u32 s52, s14, 0x19c00000
	s_addc_u32 s53, s15, 0
	s_add_u32 s54, s14, 0x18800000
	v_writelane_b32 v249, s9, 48
	s_addc_u32 s55, s15, 0
	s_ashr_i32 s9, s8, 31
	s_abs_i32 s8, s8
	s_mul_hi_u32 s6, s8, s6
	s_xor_b32 s5, s9, s5
	s_mul_i32 s9, s6, s4
	s_sub_i32 s8, s8, s9
	s_add_i32 s9, s6, 1
	s_sub_i32 s10, s8, s4
	s_cmp_ge_u32 s8, s4
	s_cselect_b32 s6, s9, s6
	s_cselect_b32 s8, s10, s8
	s_add_i32 s9, s6, 1
	s_cmp_ge_u32 s8, s4
	s_cselect_b32 s4, s9, s6
	s_xor_b32 s4, s4, s5
	s_sub_i32 s4, s4, s5
	s_mul_i32 s88, s4, s87
	s_add_i32 s4, s88, s4
	s_min_i32 s89, s4, 0xaa
	s_cmp_lt_i32 s88, s89
	v_writelane_b32 v249, s12, 50
	s_cselect_b64 s[56:57], -1, 0
	s_addk_i32 s88, 0x56
	s_addk_i32 s89, 0x55
	s_movk_i32 s20, 0x7fff
	s_mov_b32 s21, 0xffff0000
	s_movk_i32 s22, 0xbff
	v_mov_b32_e32 v115, 0x7ff
	s_mov_b32 s59, 0
	v_writelane_b32 v249, s13, 51
	s_branch .LBB0_2859

.LBB0_2858:
	s_add_i32 s4, s64, 1
	s_cmp_lt_i32 s64, 6
	s_mov_b32 s64, s4
	v_readlane_b32 s87, v249, 17
	s_waitcnt lgkmcnt(0)
	s_barrier
	s_cbranch_scc0 .LBB0_3243

.LBB0_3543:
	s_andn2_b64 vcc, exec, s[6:7]
	s_cbranch_vccz .Lp11_busy
	s_mul_i32 s75, s87, 0x180
	s_add_i32 s75, s75, 0x3fe0
	s_add_i32 s76, s75, 48
	v_readlane_b32 s7, v249, 16
	s_mov_b32 s27, s76
	s_nop 0
	s_add_i32 s25, s75, s7
	s_cmp_ge_i32 s25, s27
	s_cbranch_scc1 .Lp11_second
	v_and_b32_e32 v36, 63, v0
	v_lshrrev_b32_e32 v37, 3, v36
	v_and_b32_e32 v38, 7, v36
	v_lshlrev_b32_e32 v38, 4, v38
	v_lshl_add_u32 v82, v37, 11, v38
	v_lshl_add_u32 v83, v37, 13, v38
	v_and_b32_e32 v37, 3, v36
	v_lshrrev_b32_e32 v38, 2, v36
	v_mul_u32_u24_e32 v84, 0x820, v37
	v_lshl_add_u32 v84, v38, 2, v84
	v_lshlrev_b32_e32 v85, 4, v37
	v_lshl_add_u32 v86, v38, 11, v85
	v_lshl_add_u32 v87, v38, 9, v85
	v_mov_b32_e32 v100, 0x42800000
	v_mov_b32_e32 v101, 0x42800000
	v_readlane_b32 s8, v249, 1
	v_readlane_b32 s9, v249, 2
	s_lshl_b32 s74, s7, 1
	s_mul_i32 s74, s74, 8320
	s_add_i32 s86, s74, 8320
	s_cmp_eq_u32 s7, 7
	s_cselect_b32 s86, 0x24000, s86
	s_load_dwordx2 s[10:11], s[8:9], 0xe0
	s_mov_b32 s32, 0
	s_waitcnt lgkmcnt(0)
	s_sub_u32 s7, s25, 0x3e90
	s_lshr_b32 vcc_lo, s7, 15
	s_and_b32 s7, s7, 0x7fff
	s_lshl_b32 vcc_hi, vcc_lo, 3
	s_addk_i32 vcc_hi, 0xa8
	s_load_dwordx2 s[70:71], s[8:9], vcc_hi
	s_lshr_b32 vcc_hi, s7, 9
	s_and_b32 s7, s7, 0x1ff
	s_cmp_eq_u32 vcc_lo, 2
	s_cbranch_scc1 .Lcvdd_pdn
	s_lshr_b32 s13, s7, 4
	s_and_b32 s7, s7, 15
	s_lshl_b32 s100, vcc_hi, 21
	s_lshl_b32 s101, vcc_hi, 22
	s_lshl_b32 vcc_hi, s13, 6
	s_add_u32 s100, s100, vcc_hi
	s_lshl_b32 vcc_hi, s13, 17
	s_add_u32 s101, s101, vcc_hi
	s_lshl_b32 vcc_hi, s7, 7
	s_add_u32 s101, s101, vcc_hi
	s_lshr_b32 vcc_hi, s7, 2
	s_lshl_b32 vcc_hi, vcc_hi, 19
	s_add_u32 s100, s100, vcc_hi
	s_and_b32 vcc_hi, s7, 3
	s_lshl_b32 vcc_hi, vcc_hi, 16
	s_add_u32 s100, s100, vcc_hi
	s_lshl_b32 vcc_hi, vcc_lo, 18
	s_add_u32 s100, s100, vcc_hi
	s_add_u32 s100, s100, 0x1b000000
	s_mov_b32 s61, 0x4000
	s_mov_b32 s99, 0
	s_branch .Lcvdd_pdd

.Lcvdd_pdd:
	s_waitcnt lgkmcnt(0)
	s_add_u32 s70, s70, s101
	s_addc_u32 s71, s71, 0
	s_add_u32 s100, s10, s100
	s_addc_u32 s101, s11, 0
	s_mov_b32 m0, s74
	s_cmp_eq_u32 s99, 0
	s_cbranch_scc0 .Lcvdd_pib
	global_load_lds_dwordx4 v82, s[70:71] nt
	s_add_i32 m0, m0, 1040
	s_add_u32 s70, s70, s61
	s_addc_u32 s71, s71, 0
	global_load_lds_dwordx4 v82, s[70:71] nt
	s_add_i32 m0, m0, 1040
	s_add_u32 s70, s70, s61
	s_addc_u32 s71, s71, 0
	global_load_lds_dwordx4 v82, s[70:71] nt
	s_add_i32 m0, m0, 1040
	s_add_u32 s70, s70, s61
	s_addc_u32 s71, s71, 0
	global_load_lds_dwordx4 v82, s[70:71] nt
	s_add_i32 m0, m0, 1040
	s_add_u32 s70, s70, s61
	s_addc_u32 s71, s71, 0
	global_load_lds_dwordx4 v82, s[70:71] nt
	s_add_i32 m0, m0, 1040
	s_add_u32 s70, s70, s61
	s_addc_u32 s71, s71, 0
	global_load_lds_dwordx4 v82, s[70:71] nt
	s_add_i32 m0, m0, 1040
	s_add_u32 s70, s70, s61
	s_addc_u32 s71, s71, 0
	global_load_lds_dwordx4 v82, s[70:71] nt
	s_add_i32 m0, m0, 1040
	s_add_u32 s70, s70, s61
	s_addc_u32 s71, s71, 0
	global_load_lds_dwordx4 v82, s[70:71] nt
	s_branch .Lcvdd_pid

.Lcvdd_go:
	v_add_u32_e32 v89, s74, v84
	v_add_u32_e32 v90, 1040, v89
	ds_read2_b32 v[4:5], v89 offset0:0 offset1:32
	ds_read2_b32 v[6:7], v89 offset0:64 offset1:96
	ds_read2_b32 v[8:9], v89 offset0:128 offset1:160
	ds_read2_b32 v[10:11], v89 offset0:192 offset1:224
	ds_read2_b32 v[12:13], v90 offset0:0 offset1:32
	ds_read2_b32 v[14:15], v90 offset0:64 offset1:96
	ds_read2_b32 v[16:17], v90 offset0:128 offset1:160
	ds_read2_b32 v[18:19], v90 offset0:192 offset1:224
	ds_read2_b32 v[20:21], v89 offset0:16 offset1:48
	ds_read2_b32 v[22:23], v89 offset0:80 offset1:112
	ds_read2_b32 v[24:25], v89 offset0:144 offset1:176
	ds_read2_b32 v[26:27], v89 offset0:208 offset1:240
	ds_read2_b32 v[28:29], v90 offset0:16 offset1:48
	ds_read2_b32 v[30:31], v90 offset0:80 offset1:112
	ds_read2_b32 v[32:33], v90 offset0:144 offset1:176
	ds_read2_b32 v[34:35], v90 offset0:208 offset1:240
	s_cmp_eq_u32 s98, 0
	s_cselect_b64 vcc, -1, 0
	s_movk_i32 s7, 0x2000
	s_cselect_b32 s7, 0x8000, s7
	v_cndmask_b32_e32 v91, v87, v86, vcc
	s_waitcnt lgkmcnt(8)
	v_pk_mul_f32 v[4:5], v[4:5], v[100:101]
	v_pk_mul_f32 v[6:7], v[6:7], v[100:101]
	v_pk_mul_f32 v[8:9], v[8:9], v[100:101]
	v_pk_mul_f32 v[10:11], v[10:11], v[100:101]
	v_pk_mul_f32 v[12:13], v[12:13], v[100:101]
	v_pk_mul_f32 v[14:15], v[14:15], v[100:101]
	v_pk_mul_f32 v[16:17], v[16:17], v[100:101]
	v_pk_mul_f32 v[18:19], v[18:19], v[100:101]
	v_cvt_pk_fp8_f32 v92, v4, v5
	v_cvt_pk_fp8_f32 v93, v8, v9
	v_cvt_pk_fp8_f32 v94, v12, v13
	v_cvt_pk_fp8_f32 v95, v16, v17
	v_cvt_pk_fp8_f32 v92, v6, v7 op_sel:[0,0,1]
	v_cvt_pk_fp8_f32 v93, v10, v11 op_sel:[0,0,1]
	v_cvt_pk_fp8_f32 v94, v14, v15 op_sel:[0,0,1]
	v_cvt_pk_fp8_f32 v95, v18, v19 op_sel:[0,0,1]
	global_store_dwordx4 v91, v[92:95], s[84:85] nt
	s_waitcnt lgkmcnt(0)
	v_pk_mul_f32 v[20:21], v[20:21], v[100:101]
	v_pk_mul_f32 v[22:23], v[22:23], v[100:101]
	v_pk_mul_f32 v[24:25], v[24:25], v[100:101]
	v_pk_mul_f32 v[26:27], v[26:27], v[100:101]
	v_pk_mul_f32 v[28:29], v[28:29], v[100:101]
	v_pk_mul_f32 v[30:31], v[30:31], v[100:101]
	v_pk_mul_f32 v[32:33], v[32:33], v[100:101]
	v_pk_mul_f32 v[34:35], v[34:35], v[100:101]
	v_cvt_pk_fp8_f32 v96, v20, v21
	v_cvt_pk_fp8_f32 v97, v24, v25
	v_cvt_pk_fp8_f32 v98, v28, v29
	v_cvt_pk_fp8_f32 v99, v32, v33
	v_cvt_pk_fp8_f32 v96, v22, v23 op_sel:[0,0,1]
	v_cvt_pk_fp8_f32 v97, v26, v27 op_sel:[0,0,1]
	v_cvt_pk_fp8_f32 v98, v30, v31 op_sel:[0,0,1]
	v_cvt_pk_fp8_f32 v99, v34, v35 op_sel:[0,0,1]
	s_add_u32 s84, s84, s7
	s_addc_u32 s85, s85, 0
	global_store_dwordx4 v91, v[96:99], s[84:85] nt
	s_mov_b32 s32, 1
	s_cmp_eq_u32 s13, 0
	s_cbranch_scc1 .Lp11_second
	s_mov_b32 s25, s12
	s_mov_b32 s7, s74
	s_mov_b32 s74, s86
	s_mov_b32 s86, s7
	s_branch .Lcvdd_loop
.Lp11_second:
	s_sub_i32 s77, s87, 64
	s_mul_hi_u32 s78, s77, 0xaaaaaaab
	s_lshr_b32 s78, s78, 1
	s_mul_i32 s79, s78, 3
	s_sub_i32 s79, s77, s79
	s_mul_i32 s75, s78, 0x180
	s_lshl_b32 s79, s79, 4
	s_add_i32 s75, s75, s79
	s_add_i32 s75, s75, 0x3fe0
	s_add_i32 s76, s75, 16
	v_readlane_b32 s7, v249, 16
	s_mov_b32 s27, s76
	s_nop 0
	s_add_i32 s25, s75, s7
	s_cmp_ge_i32 s25, s27
	s_cbranch_scc1 .Lp11_done
	v_and_b32_e32 v36, 63, v0
	v_lshrrev_b32_e32 v37, 3, v36
	v_and_b32_e32 v38, 7, v36
	v_lshlrev_b32_e32 v38, 4, v38
	v_lshl_add_u32 v82, v37, 11, v38
	v_lshl_add_u32 v83, v37, 13, v38
	v_and_b32_e32 v37, 3, v36
	v_lshrrev_b32_e32 v38, 2, v36
	v_mul_u32_u24_e32 v84, 0x820, v37
	v_lshl_add_u32 v84, v38, 2, v84
	v_lshlrev_b32_e32 v85, 4, v37
	v_lshl_add_u32 v86, v38, 11, v85
	v_lshl_add_u32 v87, v38, 9, v85
	v_mov_b32_e32 v100, 0x42800000
	v_mov_b32_e32 v101, 0x42800000
	v_readlane_b32 s8, v249, 1
	v_readlane_b32 s9, v249, 2
	s_lshl_b32 s74, s7, 1
	s_mul_i32 s74, s74, 8320
	s_add_i32 s86, s74, 8320
	s_cmp_eq_u32 s7, 7
	s_cselect_b32 s86, 0x24000, s86
	s_load_dwordx2 s[10:11], s[8:9], 0xe0
	s_mov_b32 s32, 0
	s_waitcnt lgkmcnt(0)
	s_sub_u32 s7, s25, 0x3e90
	s_lshr_b32 vcc_lo, s7, 15
	s_and_b32 s7, s7, 0x7fff
	s_lshl_b32 vcc_hi, vcc_lo, 3
	s_addk_i32 vcc_hi, 0xa8
	s_load_dwordx2 s[70:71], s[8:9], vcc_hi
	s_lshr_b32 vcc_hi, s7, 9
	s_and_b32 s7, s7, 0x1ff
	s_cmp_eq_u32 vcc_lo, 2
	s_cbranch_scc1 .Lcvde_pdn
	s_lshr_b32 s13, s7, 4
	s_and_b32 s7, s7, 15
	s_lshl_b32 s100, vcc_hi, 21
	s_lshl_b32 s101, vcc_hi, 22
	s_lshl_b32 vcc_hi, s13, 6
	s_add_u32 s100, s100, vcc_hi
	s_lshl_b32 vcc_hi, s13, 17
	s_add_u32 s101, s101, vcc_hi
	s_lshl_b32 vcc_hi, s7, 7
	s_add_u32 s101, s101, vcc_hi
	s_lshr_b32 vcc_hi, s7, 2
	s_lshl_b32 vcc_hi, vcc_hi, 19
	s_add_u32 s100, s100, vcc_hi
	s_and_b32 vcc_hi, s7, 3
	s_lshl_b32 vcc_hi, vcc_hi, 16
	s_add_u32 s100, s100, vcc_hi
	s_lshl_b32 vcc_hi, vcc_lo, 18
	s_add_u32 s100, s100, vcc_hi
	s_add_u32 s100, s100, 0x1b000000
	s_mov_b32 s61, 0x4000
	s_mov_b32 s99, 0
	s_branch .Lcvde_pdd

.Lp11_busy:
	v_ashrrev_i32_e32 v2, 31, v6
	v_lshrrev_b32_e32 v2, 26, v2
	v_add_u32_e32 v2, v6, v2
	v_ashrrev_i32_e32 v7, 6, v2
	v_bfe_i32 v2, v6, 27, 1
	v_readlane_b32 s2, v249, 1
	v_lshlrev_b32_e32 v1, 4, v6
	v_lshrrev_b32_e32 v2, 22, v2
	v_readlane_b32 s3, v249, 2
	v_add_u32_e32 v2, v1, v2
	s_load_dwordx4 s[12:15], s[2:3], 0xd8
	v_and_b32_e32 v2, 0xfffffc00, v2
	v_sub_u32_e32 v1, v1, v2
	v_lshrrev_b32_e32 v2, 4, v1
	v_bitop3_b32 v2, v2, v1, 32 bitop3:0x6c
	v_ashrrev_i32_e32 v1, 31, v1
	v_lshrrev_b32_e32 v1, 26, v1
	s_waitcnt lgkmcnt(0)
	s_add_u32 s2, s14, 0xb600000
	v_add_u32_e32 v1, v2, v1
	s_addc_u32 s3, s15, 0
	v_ashrrev_i32_e32 v8, 6, v1
	s_add_u32 s10, s14, 0xb400000
	v_mul_i32_i24_e32 v4, 64, v8
	s_addc_u32 s11, s15, 0
	v_sub_u32_e32 v2, v2, v4
	v_mov_b32_e32 v4, 1
	s_ashr_i32 s16, s8, 6
	s_ashr_i32 s5, s4, 31
	s_ashr_i32 s9, s8, 8
	v_lshlrev_b32_e32 v3, 3, v7
	v_lshlrev_b32_e32 v1, 5, v7
	v_ashrrev_i16_sdwa v2, v4, sext(v2) dst_sel:DWORD dst_unused:UNUSED_PAD src0_sel:DWORD src1_sel:BYTE_0
	s_lshl_b32 s33, s16, 10
	s_lshl_b64 s[6:7], s[4:5], 12
	v_and_b32_e32 v3, 0xffff0, v3
	v_and_b32_e32 v1, 32, v1
	v_bfe_i32 v9, v2, 0, 16
	s_add_u32 s6, s2, s6
	v_add_u32_e32 v1, v1, v9
	v_add_lshl_u32 v2, v8, v3, 12
	s_addc_u32 s7, s3, s7
	s_add_i32 s34, s33, 0
	v_lshl_add_u32 v130, v1, 1, v2
	s_add_i32 m0, s34, 0x10000
	v_add_u32_e32 v132, 0x40000, v130
	global_load_lds_dwordx4 v130, s[10:11]
	s_add_i32 m0, s34, 0x12000
	s_add_u32 s12, s14, 0xb480000
	global_load_lds_dwordx4 v132, s[10:11]
	s_addc_u32 s13, s15, 0
	s_add_i32 m0, s34, 0x14000
	s_add_i32 s35, s34, 0x2000
	global_load_lds_dwordx4 v130, s[12:13]
	s_add_i32 m0, s34, 0x16000
	v_mov_b32_e32 v131, 0
	global_load_lds_dwordx4 v132, s[12:13]
	s_mov_b32 m0, s34
	s_add_u32 s12, s6, 0x80000
	global_load_lds_dwordx4 v130, s[6:7]
	s_mov_b32 m0, s35
	s_addc_u32 s13, s7, 0
	s_add_i32 s36, s34, 0x4000
	global_load_lds_dwordx4 v132, s[6:7]
	s_mov_b32 m0, s36
	s_add_i32 s37, s34, 0x6000
	global_load_lds_dwordx4 v130, s[12:13]
	s_mov_b32 m0, s37
	v_mov_b32_e32 v133, v131
	global_load_lds_dwordx4 v132, s[12:13]
	s_cmp_eq_u32 s9, 1
	s_mov_b32 s38, 0
	v_lshl_add_u64 v[2:3], s[6:7], 0, v[130:131]
	s_cselect_b64 s[12:13], -1, 0
	s_cmp_lg_u32 s9, 1
	v_lshl_add_u64 v[4:5], s[6:7], 0, v[132:133]
	s_cbranch_scc1 .LBB0_3546
	s_barrier
